# GEMM MMA segments: dropped the back-to-back s_setprio 0 / s_setprio 1 pair in the middle of each 32-MFMA segment (28 sites)
# speedup vs baseline: 1.0061x; 1.0061x over previous
.LBB0_161:
	s_waitcnt vmcnt(8)
	s_add_u32 s40, s36, 0x80
	s_waitcnt lgkmcnt(0)
	s_addc_u32 s41, s37, 0
	s_and_b64 s[38:39], s[38:39], exec
	s_cselect_b32 s41, s17, s41
	s_cselect_b32 s40, s16, s40
	s_cselect_b32 s39, s29, s74
	s_cselect_b32 s38, s72, s73
	s_barrier
	s_setprio 1
	s_waitcnt lgkmcnt(0)
	v_mfma_f32_16x16x32_bf16 v[72:75], v[152:155], v[192:195], v[72:75]
	v_mfma_f32_16x16x32_bf16 v[68:71], v[160:163], v[192:195], v[68:71]
	v_mfma_f32_16x16x32_bf16 v[60:63], v[152:155], v[184:187], v[60:63]
	v_mfma_f32_16x16x32_bf16 v[56:59], v[160:163], v[184:187], v[56:59]
	v_mfma_f32_16x16x32_bf16 v[52:55], v[152:155], v[176:179], v[52:55]
	v_mfma_f32_16x16x32_bf16 v[48:51], v[160:163], v[176:179], v[48:51]
	v_mfma_f32_16x16x32_bf16 v[44:47], v[152:155], v[168:171], v[44:47]
	v_mfma_f32_16x16x32_bf16 v[40:43], v[160:163], v[168:171], v[40:43]
	v_mfma_f32_16x16x32_bf16 v[72:75], v[156:159], v[196:199], v[72:75]
	v_mfma_f32_16x16x32_bf16 v[68:71], v[164:167], v[196:199], v[68:71]
	v_mfma_f32_16x16x32_bf16 v[60:63], v[156:159], v[188:191], v[60:63]
	v_mfma_f32_16x16x32_bf16 v[56:59], v[164:167], v[188:191], v[56:59]
	v_mfma_f32_16x16x32_bf16 v[52:55], v[156:159], v[180:183], v[52:55]
	v_mfma_f32_16x16x32_bf16 v[48:51], v[164:167], v[180:183], v[48:51]
	v_mfma_f32_16x16x32_bf16 v[44:47], v[156:159], v[172:175], v[44:47]
	v_mfma_f32_16x16x32_bf16 v[40:43], v[164:167], v[172:175], v[40:43]
	v_mfma_f32_16x16x32_bf16 v[132:135], v[136:139], v[192:195], v[132:135]
	v_mfma_f32_16x16x32_bf16 v[128:131], v[144:147], v[192:195], v[128:131]
	v_mfma_f32_16x16x32_bf16 v[124:127], v[136:139], v[184:187], v[124:127]
	v_mfma_f32_16x16x32_bf16 v[120:123], v[144:147], v[184:187], v[120:123]
	v_mfma_f32_16x16x32_bf16 v[116:119], v[136:139], v[176:179], v[116:119]
	v_mfma_f32_16x16x32_bf16 v[112:115], v[144:147], v[176:179], v[112:115]
	v_mfma_f32_16x16x32_bf16 v[108:111], v[136:139], v[168:171], v[108:111]
	v_mfma_f32_16x16x32_bf16 v[104:107], v[144:147], v[168:171], v[104:107]
	v_mfma_f32_16x16x32_bf16 v[132:135], v[140:143], v[196:199], v[132:135]
	v_mfma_f32_16x16x32_bf16 v[128:131], v[148:151], v[196:199], v[128:131]
	v_mfma_f32_16x16x32_bf16 v[124:127], v[140:143], v[188:191], v[124:127]
	v_mfma_f32_16x16x32_bf16 v[120:123], v[148:151], v[188:191], v[120:123]
	v_mfma_f32_16x16x32_bf16 v[116:119], v[140:143], v[180:183], v[116:119]
	v_mfma_f32_16x16x32_bf16 v[112:115], v[148:151], v[180:183], v[112:115]
	v_mfma_f32_16x16x32_bf16 v[108:111], v[140:143], v[172:175], v[108:111]
	v_mfma_f32_16x16x32_bf16 v[104:107], v[148:151], v[172:175], v[104:107]
	s_setprio 0
	s_barrier
	s_mov_b32 m0, s51
	v_lshl_add_u64 v[4:5], s[38:39], 0, v[200:201]
	s_add_u32 s76, s38, 0x80000
	ds_read_b128 v[168:171], v234 offset:16384
	ds_read_b128 v[172:175], v234 offset:17408
	ds_read_b128 v[176:179], v234 offset:18432
	ds_read_b128 v[180:183], v234 offset:19456
	ds_read_b128 v[184:187], v234 offset:20480
	ds_read_b128 v[188:191], v234 offset:21504
	ds_read_b128 v[192:195], v234 offset:22528
	ds_read_b128 v[196:199], v234 offset:23552
	global_load_lds_dwordx4 v[4:5], off
	v_lshl_add_u64 v[236:237], s[38:39], 0, v[202:203]
	s_mov_b32 m0, s52
	s_addc_u32 s77, s39, 0
	global_load_lds_dwordx4 v[236:237], off
	v_lshl_add_u64 v[238:239], s[76:77], 0, v[200:201]
	s_mov_b32 m0, s53
	v_mov_b32_e32 v205, v3
	global_load_lds_dwordx4 v[238:239], off
	v_lshl_add_u64 v[238:239], s[76:77], 0, v[202:203]
	s_mov_b32 m0, s54
	v_lshl_add_u64 v[240:241], s[40:41], 0, v[204:205]
	global_load_lds_dwordx4 v[238:239], off
	s_mov_b32 m0, s35
	v_lshl_add_u64 v[238:239], s[40:41], 0, v[2:3]
	global_load_lds_dwordx4 v2, s[40:41]
	s_mov_b32 m0, s55
	s_nop 0
	global_load_lds_dwordx4 v204, s[40:41]
	s_waitcnt vmcnt(8)
	s_waitcnt lgkmcnt(0)
	s_barrier
	s_setprio 1
	s_waitcnt lgkmcnt(0)
	v_mfma_f32_16x16x32_bf16 v[36:39], v[152:155], v[168:171], v[36:39]
	v_mfma_f32_16x16x32_bf16 v[32:35], v[160:163], v[168:171], v[32:35]
	v_mfma_f32_16x16x32_bf16 v[28:31], v[152:155], v[176:179], v[28:31]
	v_mfma_f32_16x16x32_bf16 v[24:27], v[160:163], v[176:179], v[24:27]
	v_mfma_f32_16x16x32_bf16 v[20:23], v[152:155], v[184:187], v[20:23]
	v_mfma_f32_16x16x32_bf16 v[16:19], v[160:163], v[184:187], v[16:19]
	v_mfma_f32_16x16x32_bf16 v[12:15], v[152:155], v[192:195], v[12:15]
	v_mfma_f32_16x16x32_bf16 v[8:11], v[160:163], v[192:195], v[8:11]
	v_mfma_f32_16x16x32_bf16 v[36:39], v[156:159], v[172:175], v[36:39]
	v_mfma_f32_16x16x32_bf16 v[32:35], v[164:167], v[172:175], v[32:35]
	v_mfma_f32_16x16x32_bf16 v[28:31], v[156:159], v[180:183], v[28:31]
	v_mfma_f32_16x16x32_bf16 v[24:27], v[164:167], v[180:183], v[24:27]
	v_mfma_f32_16x16x32_bf16 v[20:23], v[156:159], v[188:191], v[20:23]
	v_mfma_f32_16x16x32_bf16 v[16:19], v[164:167], v[188:191], v[16:19]
	v_mfma_f32_16x16x32_bf16 v[12:15], v[156:159], v[196:199], v[12:15]
	v_mfma_f32_16x16x32_bf16 v[8:11], v[164:167], v[196:199], v[8:11]
	v_mfma_f32_16x16x32_bf16 v[92:95], v[136:139], v[168:171], v[92:95]
	v_mfma_f32_16x16x32_bf16 v[88:91], v[144:147], v[168:171], v[88:91]
	v_mfma_f32_16x16x32_bf16 v[76:79], v[136:139], v[176:179], v[76:79]
	v_mfma_f32_16x16x32_bf16 v[64:67], v[144:147], v[176:179], v[64:67]
	v_mfma_f32_16x16x32_bf16 v[100:103], v[136:139], v[184:187], v[100:103]
	v_mfma_f32_16x16x32_bf16 v[96:99], v[144:147], v[184:187], v[96:99]
	v_mfma_f32_16x16x32_bf16 v[84:87], v[136:139], v[192:195], v[84:87]
	v_mfma_f32_16x16x32_bf16 v[80:83], v[144:147], v[192:195], v[80:83]
	v_mfma_f32_16x16x32_bf16 v[92:95], v[140:143], v[172:175], v[92:95]
	v_mfma_f32_16x16x32_bf16 v[88:91], v[148:151], v[172:175], v[88:91]
	v_mfma_f32_16x16x32_bf16 v[76:79], v[140:143], v[180:183], v[76:79]
	v_mfma_f32_16x16x32_bf16 v[64:67], v[148:151], v[180:183], v[64:67]
	v_mfma_f32_16x16x32_bf16 v[100:103], v[140:143], v[188:191], v[100:103]
	v_mfma_f32_16x16x32_bf16 v[96:99], v[148:151], v[188:191], v[96:99]
	v_mfma_f32_16x16x32_bf16 v[84:87], v[140:143], v[196:199], v[84:87]
	v_mfma_f32_16x16x32_bf16 v[80:83], v[148:151], v[196:199], v[80:83]
	s_setprio 0
	s_barrier
	s_add_i32 s76, 0, 0x18000
	v_add_u32_e32 v7, s76, v230
	s_add_i32 s77, 0, 0x1c000
	ds_read_b128 v[136:139], v7
	ds_read_b128 v[140:143], v7 offset:1024
	ds_read_b128 v[144:147], v7 offset:2048
	ds_read_b128 v[148:151], v7 offset:3072
	v_add_u32_e32 v7, s77, v230
	ds_read_b128 v[152:155], v7
	ds_read_b128 v[156:159], v7 offset:1024
	ds_read_b128 v[160:163], v7 offset:2048
	ds_read_b128 v[164:167], v7 offset:3072
	s_mov_b32 m0, s56
	v_lshl_add_u64 v[216:217], s[40:41], 0, v[216:217]
	ds_read_b128 v[168:171], v234 offset:32768
	ds_read_b128 v[172:175], v234 offset:33792
	ds_read_b128 v[176:179], v234 offset:34816
	ds_read_b128 v[180:183], v234 offset:35840
	ds_read_b128 v[184:187], v234 offset:36864
	ds_read_b128 v[188:191], v234 offset:37888
	ds_read_b128 v[192:195], v234 offset:38912
	ds_read_b128 v[196:199], v234 offset:39936
	global_load_lds_dwordx4 v[216:217], off
	v_lshl_add_u64 v[214:215], s[40:41], 0, v[214:215]
	s_mov_b32 m0, s57
	s_nop 0
	global_load_lds_dwordx4 v[214:215], off
	s_waitcnt vmcnt(8)
	s_waitcnt lgkmcnt(0)
	s_barrier
	s_setprio 1
	s_waitcnt lgkmcnt(0)
	v_mfma_f32_16x16x32_bf16 v[72:75], v[136:139], v[168:171], v[72:75]
	v_mfma_f32_16x16x32_bf16 v[68:71], v[144:147], v[168:171], v[68:71]
	v_mfma_f32_16x16x32_bf16 v[60:63], v[136:139], v[176:179], v[60:63]
	v_mfma_f32_16x16x32_bf16 v[56:59], v[144:147], v[176:179], v[56:59]
	v_mfma_f32_16x16x32_bf16 v[52:55], v[136:139], v[184:187], v[52:55]
	v_mfma_f32_16x16x32_bf16 v[48:51], v[144:147], v[184:187], v[48:51]
	v_mfma_f32_16x16x32_bf16 v[44:47], v[136:139], v[192:195], v[44:47]
	v_mfma_f32_16x16x32_bf16 v[40:43], v[144:147], v[192:195], v[40:43]
	v_mfma_f32_16x16x32_bf16 v[72:75], v[140:143], v[172:175], v[72:75]
	v_mfma_f32_16x16x32_bf16 v[68:71], v[148:151], v[172:175], v[68:71]
	v_mfma_f32_16x16x32_bf16 v[60:63], v[140:143], v[180:183], v[60:63]
	v_mfma_f32_16x16x32_bf16 v[56:59], v[148:151], v[180:183], v[56:59]
	v_mfma_f32_16x16x32_bf16 v[52:55], v[140:143], v[188:191], v[52:55]
	v_mfma_f32_16x16x32_bf16 v[48:51], v[148:151], v[188:191], v[48:51]
	v_mfma_f32_16x16x32_bf16 v[44:47], v[140:143], v[196:199], v[44:47]
	v_mfma_f32_16x16x32_bf16 v[40:43], v[148:151], v[196:199], v[40:43]
	v_mfma_f32_16x16x32_bf16 v[132:135], v[152:155], v[168:171], v[132:135]
	v_mfma_f32_16x16x32_bf16 v[128:131], v[160:163], v[168:171], v[128:131]
	v_mfma_f32_16x16x32_bf16 v[124:127], v[152:155], v[176:179], v[124:127]
	v_mfma_f32_16x16x32_bf16 v[120:123], v[160:163], v[176:179], v[120:123]
	v_mfma_f32_16x16x32_bf16 v[116:119], v[152:155], v[184:187], v[116:119]
	v_mfma_f32_16x16x32_bf16 v[112:115], v[160:163], v[184:187], v[112:115]
	v_mfma_f32_16x16x32_bf16 v[108:111], v[152:155], v[192:195], v[108:111]
	v_mfma_f32_16x16x32_bf16 v[104:107], v[160:163], v[192:195], v[104:107]
	v_mfma_f32_16x16x32_bf16 v[132:135], v[156:159], v[172:175], v[132:135]
	v_mfma_f32_16x16x32_bf16 v[128:131], v[164:167], v[172:175], v[128:131]
	v_mfma_f32_16x16x32_bf16 v[124:127], v[156:159], v[180:183], v[124:127]
	v_mfma_f32_16x16x32_bf16 v[120:123], v[164:167], v[180:183], v[120:123]
	v_mfma_f32_16x16x32_bf16 v[116:119], v[156:159], v[188:191], v[116:119]
	v_mfma_f32_16x16x32_bf16 v[112:115], v[164:167], v[188:191], v[112:115]
	v_mfma_f32_16x16x32_bf16 v[108:111], v[156:159], v[196:199], v[108:111]
	v_mfma_f32_16x16x32_bf16 v[104:107], v[164:167], v[196:199], v[104:107]
	s_setprio 0
	s_barrier
	s_add_i32 s40, s76, s50
	v_lshl_add_u64 v[4:5], v[4:5], 0, s[20:21]
	s_mov_b32 m0, s40
	ds_read_b128 v[168:171], v234 offset:49152
	ds_read_b128 v[172:175], v234 offset:50176
	ds_read_b128 v[176:179], v234 offset:51200
	ds_read_b128 v[180:183], v234 offset:52224
	ds_read_b128 v[184:187], v234 offset:53248
	ds_read_b128 v[188:191], v234 offset:54272
	ds_read_b128 v[192:195], v234 offset:55296
	ds_read_b128 v[196:199], v234 offset:56320
	global_load_lds_dwordx4 v[4:5], off
	s_add_i32 m0, s40, 0x2000
	s_add_u32 s38, s38, 0x80080
	v_lshl_add_u64 v[4:5], v[236:237], 0, s[20:21]
	s_addc_u32 s39, s39, 0
	s_add_i32 s40, s77, s50
	global_load_lds_dwordx4 v[4:5], off
	v_lshl_add_u64 v[4:5], s[38:39], 0, v[200:201]
	s_mov_b32 m0, s40
	s_nop 0
	global_load_lds_dwordx4 v[4:5], off
	v_lshl_add_u64 v[4:5], s[38:39], 0, v[202:203]
	s_add_i32 m0, s40, 0x2000
	s_nop 0
	global_load_lds_dwordx4 v[4:5], off
	v_lshl_add_u64 v[4:5], v[238:239], 0, s[20:21]
	s_mov_b32 m0, s60
	s_nop 0
	global_load_lds_dwordx4 v[4:5], off
	v_lshl_add_u64 v[4:5], v[240:241], 0, s[20:21]
	s_mov_b32 m0, s61
	s_nop 0
	global_load_lds_dwordx4 v[4:5], off
	s_waitcnt vmcnt(8)
	s_waitcnt lgkmcnt(0)
	s_barrier
	s_setprio 1
	s_waitcnt lgkmcnt(0)
	v_mfma_f32_16x16x32_bf16 v[36:39], v[136:139], v[168:171], v[36:39]
	v_mfma_f32_16x16x32_bf16 v[32:35], v[144:147], v[168:171], v[32:35]
	v_mfma_f32_16x16x32_bf16 v[28:31], v[136:139], v[176:179], v[28:31]
	v_mfma_f32_16x16x32_bf16 v[24:27], v[144:147], v[176:179], v[24:27]
	v_mfma_f32_16x16x32_bf16 v[20:23], v[136:139], v[184:187], v[20:23]
	v_mfma_f32_16x16x32_bf16 v[16:19], v[144:147], v[184:187], v[16:19]
	v_mfma_f32_16x16x32_bf16 v[12:15], v[136:139], v[192:195], v[12:15]
	v_mfma_f32_16x16x32_bf16 v[8:11], v[144:147], v[192:195], v[8:11]
	v_mfma_f32_16x16x32_bf16 v[36:39], v[140:143], v[172:175], v[36:39]
	v_mfma_f32_16x16x32_bf16 v[32:35], v[148:151], v[172:175], v[32:35]
	v_mfma_f32_16x16x32_bf16 v[28:31], v[140:143], v[180:183], v[28:31]
	v_mfma_f32_16x16x32_bf16 v[24:27], v[148:151], v[180:183], v[24:27]
	v_mfma_f32_16x16x32_bf16 v[20:23], v[140:143], v[188:191], v[20:23]
	v_mfma_f32_16x16x32_bf16 v[16:19], v[148:151], v[188:191], v[16:19]
	v_mfma_f32_16x16x32_bf16 v[12:15], v[140:143], v[196:199], v[12:15]
	v_mfma_f32_16x16x32_bf16 v[8:11], v[148:151], v[196:199], v[8:11]
	v_mfma_f32_16x16x32_bf16 v[92:95], v[152:155], v[168:171], v[92:95]
	v_mfma_f32_16x16x32_bf16 v[88:91], v[160:163], v[168:171], v[88:91]
	v_mfma_f32_16x16x32_bf16 v[76:79], v[152:155], v[176:179], v[76:79]
	v_mfma_f32_16x16x32_bf16 v[64:67], v[160:163], v[176:179], v[64:67]
	v_mfma_f32_16x16x32_bf16 v[100:103], v[152:155], v[184:187], v[100:103]
	v_mfma_f32_16x16x32_bf16 v[96:99], v[160:163], v[184:187], v[96:99]
	v_mfma_f32_16x16x32_bf16 v[84:87], v[152:155], v[192:195], v[84:87]
	v_mfma_f32_16x16x32_bf16 v[80:83], v[160:163], v[192:195], v[80:83]
	v_mfma_f32_16x16x32_bf16 v[92:95], v[156:159], v[172:175], v[92:95]
	v_mfma_f32_16x16x32_bf16 v[88:91], v[164:167], v[172:175], v[88:91]
	v_mfma_f32_16x16x32_bf16 v[76:79], v[156:159], v[180:183], v[76:79]
	v_mfma_f32_16x16x32_bf16 v[64:67], v[164:167], v[180:183], v[64:67]
	v_mfma_f32_16x16x32_bf16 v[100:103], v[156:159], v[188:191], v[100:103]
	v_mfma_f32_16x16x32_bf16 v[96:99], v[164:167], v[188:191], v[96:99]
	v_mfma_f32_16x16x32_bf16 v[84:87], v[156:159], v[196:199], v[84:87]
	v_mfma_f32_16x16x32_bf16 v[80:83], v[164:167], v[196:199], v[80:83]
	s_setprio 0
	s_barrier
	s_add_i32 s75, s75, 2
	s_add_u32 s36, s36, 0x100
	s_addc_u32 s37, s37, 0
	s_add_u32 s73, s73, 0x100
	s_addc_u32 s74, s74, 0
	s_cmp_gt_u32 s75, 29
	s_cbranch_scc1 .LBB0_164

.LBB0_216:
	s_waitcnt vmcnt(8)
	s_add_u32 s42, s38, 0x80
	s_waitcnt lgkmcnt(0)
	s_addc_u32 s43, s39, 0
	s_and_b64 s[40:41], s[40:41], exec
	s_cselect_b32 s43, s19, s43
	s_cselect_b32 s42, s18, s42
	s_cselect_b32 s41, s31, s77
	s_cselect_b32 s40, s75, s76
	s_barrier
	s_setprio 1
	s_waitcnt lgkmcnt(0)
	v_mfma_scale_f32_16x16x128_f8f6f4 v[132:135], v[26:33], v[58:65], v[132:135], v216, v216 op_sel_hi:[0,0,0]
	v_mfma_scale_f32_16x16x128_f8f6f4 v[128:131], v[18:25], v[58:65], v[128:131], v216, v216 op_sel_hi:[0,0,0]
	v_mfma_scale_f32_16x16x128_f8f6f4 v[124:127], v[26:33], v[50:57], v[124:127], v216, v216 op_sel_hi:[0,0,0]
	v_mfma_scale_f32_16x16x128_f8f6f4 v[120:123], v[18:25], v[50:57], v[120:123], v216, v216 op_sel_hi:[0,0,0]
	v_mfma_scale_f32_16x16x128_f8f6f4 v[116:119], v[26:33], v[42:49], v[116:119], v216, v216 op_sel_hi:[0,0,0]
	v_mfma_scale_f32_16x16x128_f8f6f4 v[112:115], v[18:25], v[42:49], v[112:115], v216, v216 op_sel_hi:[0,0,0]
	v_mfma_scale_f32_16x16x128_f8f6f4 v[108:111], v[26:33], v[34:41], v[108:111], v216, v216 op_sel_hi:[0,0,0]
	v_mfma_scale_f32_16x16x128_f8f6f4 v[104:107], v[18:25], v[34:41], v[104:107], v216, v216 op_sel_hi:[0,0,0]
	v_mfma_scale_f32_16x16x128_f8f6f4 v[196:199], v[10:17], v[58:65], v[196:199], v216, v216 op_sel_hi:[0,0,0]
	v_mfma_scale_f32_16x16x128_f8f6f4 v[192:195], v[2:9], v[58:65], v[192:195], v216, v216 op_sel_hi:[0,0,0]
	v_mfma_scale_f32_16x16x128_f8f6f4 v[188:191], v[10:17], v[50:57], v[188:191], v216, v216 op_sel_hi:[0,0,0]
	v_mfma_scale_f32_16x16x128_f8f6f4 v[184:187], v[2:9], v[50:57], v[184:187], v216, v216 op_sel_hi:[0,0,0]
	v_mfma_scale_f32_16x16x128_f8f6f4 v[180:183], v[10:17], v[42:49], v[180:183], v216, v216 op_sel_hi:[0,0,0]
	v_mfma_scale_f32_16x16x128_f8f6f4 v[176:179], v[2:9], v[42:49], v[176:179], v216, v216 op_sel_hi:[0,0,0]
	v_mfma_scale_f32_16x16x128_f8f6f4 v[172:175], v[10:17], v[34:41], v[172:175], v216, v216 op_sel_hi:[0,0,0]
	v_mfma_scale_f32_16x16x128_f8f6f4 v[168:171], v[2:9], v[34:41], v[168:171], v216, v216 op_sel_hi:[0,0,0]
	s_setprio 0
	s_barrier
	s_mov_b32 m0, s51
	v_lshl_add_u64 v[34:35], s[40:41], 0, v[200:201]
	s_add_u32 s80, s40, 0x40000
	ds_read_b128 v[42:45], v219 offset:16384
	ds_read_b128 v[46:49], v219 offset:17408
	ds_read_b128 v[50:53], v219 offset:18432
	ds_read_b128 v[54:57], v219 offset:19456
	ds_read_b128 v[58:61], v219 offset:20480
	ds_read_b128 v[62:65], v219 offset:21504
	ds_read_b128 v[240:243], v219 offset:22528
	ds_read_b128 v[244:247], v219 offset:23552
	global_load_lds_dwordx4 v[34:35], off
	v_lshl_add_u64 v[36:37], s[40:41], 0, v[202:203]
	s_mov_b32 m0, s52
	s_addc_u32 s81, s41, 0
	global_load_lds_dwordx4 v[36:37], off
	v_lshl_add_u64 v[38:39], s[80:81], 0, v[200:201]
	s_mov_b32 m0, s53
	v_mov_b32_e32 v205, v67
	global_load_lds_dwordx4 v[38:39], off
	v_lshl_add_u64 v[38:39], s[80:81], 0, v[202:203]
	s_mov_b32 m0, s54
	v_lshl_add_u64 v[40:41], s[42:43], 0, v[66:67]
	global_load_lds_dwordx4 v[38:39], off
	s_mov_b32 m0, s37
	v_lshl_add_u64 v[38:39], s[42:43], 0, v[204:205]
	global_load_lds_dwordx4 v66, s[42:43]
	s_mov_b32 m0, s55
	s_nop 0
	global_load_lds_dwordx4 v204, s[42:43]
	s_waitcnt vmcnt(8)
	s_waitcnt lgkmcnt(0)
	s_barrier
	s_setprio 1
	s_waitcnt lgkmcnt(0)
	v_mfma_scale_f32_16x16x128_f8f6f4 v[100:103], v[26:33], v[42:49], v[100:103], v216, v216 op_sel_hi:[0,0,0]
	v_mfma_scale_f32_16x16x128_f8f6f4 v[96:99], v[18:25], v[42:49], v[96:99], v216, v216 op_sel_hi:[0,0,0]
	v_mfma_scale_f32_16x16x128_f8f6f4 v[92:95], v[26:33], v[50:57], v[92:95], v216, v216 op_sel_hi:[0,0,0]
	v_mfma_scale_f32_16x16x128_f8f6f4 v[88:91], v[18:25], v[50:57], v[88:91], v216, v216 op_sel_hi:[0,0,0]
	v_mfma_scale_f32_16x16x128_f8f6f4 v[84:87], v[26:33], v[58:65], v[84:87], v216, v216 op_sel_hi:[0,0,0]
	v_mfma_scale_f32_16x16x128_f8f6f4 v[80:83], v[18:25], v[58:65], v[80:83], v216, v216 op_sel_hi:[0,0,0]
	v_mfma_scale_f32_16x16x128_f8f6f4 v[76:79], v[26:33], v[240:247], v[76:79], v216, v216 op_sel_hi:[0,0,0]
	v_mfma_scale_f32_16x16x128_f8f6f4 v[72:75], v[18:25], v[240:247], v[72:75], v216, v216 op_sel_hi:[0,0,0]
	v_mfma_scale_f32_16x16x128_f8f6f4 v[164:167], v[10:17], v[42:49], v[164:167], v216, v216 op_sel_hi:[0,0,0]
	v_mfma_scale_f32_16x16x128_f8f6f4 v[160:163], v[2:9], v[42:49], v[160:163], v216, v216 op_sel_hi:[0,0,0]
	v_mfma_scale_f32_16x16x128_f8f6f4 v[148:151], v[10:17], v[50:57], v[148:151], v216, v216 op_sel_hi:[0,0,0]
	v_mfma_scale_f32_16x16x128_f8f6f4 v[136:139], v[2:9], v[50:57], v[136:139], v216, v216 op_sel_hi:[0,0,0]
	v_mfma_scale_f32_16x16x128_f8f6f4 v[156:159], v[10:17], v[58:65], v[156:159], v216, v216 op_sel_hi:[0,0,0]
	v_mfma_scale_f32_16x16x128_f8f6f4 v[152:155], v[2:9], v[58:65], v[152:155], v216, v216 op_sel_hi:[0,0,0]
	v_mfma_scale_f32_16x16x128_f8f6f4 v[144:147], v[10:17], v[240:247], v[144:147], v216, v216 op_sel_hi:[0,0,0]
	v_mfma_scale_f32_16x16x128_f8f6f4 v[140:143], v[2:9], v[240:247], v[140:143], v216, v216 op_sel_hi:[0,0,0]
	s_setprio 0
	s_barrier
	ds_read_b128 v[2:5], v232
	ds_read_b128 v[6:9], v233
	ds_read_b128 v[10:13], v234
	ds_read_b128 v[14:17], v235
	ds_read_b128 v[18:21], v236
	ds_read_b128 v[22:25], v237
	ds_read_b128 v[26:29], v238
	ds_read_b128 v[30:33], v239
	s_mov_b32 m0, s56
	v_lshl_add_u64 v[68:69], s[42:43], 0, v[214:215]
	ds_read_b128 v[42:45], v219 offset:32768
	ds_read_b128 v[46:49], v219 offset:33792
	ds_read_b128 v[50:53], v219 offset:34816
	ds_read_b128 v[54:57], v219 offset:35840
	ds_read_b128 v[58:61], v219 offset:36864
	ds_read_b128 v[62:65], v219 offset:37888
	ds_read_b128 v[240:243], v219 offset:38912
	ds_read_b128 v[244:247], v219 offset:39936
	global_load_lds_dwordx4 v[68:69], off
	v_lshl_add_u64 v[68:69], s[42:43], 0, v[212:213]
	s_mov_b32 m0, s57
	s_nop 0
	global_load_lds_dwordx4 v[68:69], off
	s_waitcnt vmcnt(8)
	s_waitcnt lgkmcnt(0)
	s_barrier
	s_setprio 1
	s_waitcnt lgkmcnt(0)
	v_mfma_scale_f32_16x16x128_f8f6f4 v[132:135], v[2:9], v[42:49], v[132:135], v216, v216 op_sel_hi:[0,0,0]
	v_mfma_scale_f32_16x16x128_f8f6f4 v[128:131], v[10:17], v[42:49], v[128:131], v216, v216 op_sel_hi:[0,0,0]
	v_mfma_scale_f32_16x16x128_f8f6f4 v[124:127], v[2:9], v[50:57], v[124:127], v216, v216 op_sel_hi:[0,0,0]
	v_mfma_scale_f32_16x16x128_f8f6f4 v[120:123], v[10:17], v[50:57], v[120:123], v216, v216 op_sel_hi:[0,0,0]
	v_mfma_scale_f32_16x16x128_f8f6f4 v[116:119], v[2:9], v[58:65], v[116:119], v216, v216 op_sel_hi:[0,0,0]
	v_mfma_scale_f32_16x16x128_f8f6f4 v[112:115], v[10:17], v[58:65], v[112:115], v216, v216 op_sel_hi:[0,0,0]
	v_mfma_scale_f32_16x16x128_f8f6f4 v[108:111], v[2:9], v[240:247], v[108:111], v216, v216 op_sel_hi:[0,0,0]
	v_mfma_scale_f32_16x16x128_f8f6f4 v[104:107], v[10:17], v[240:247], v[104:107], v216, v216 op_sel_hi:[0,0,0]
	v_mfma_scale_f32_16x16x128_f8f6f4 v[196:199], v[18:25], v[42:49], v[196:199], v216, v216 op_sel_hi:[0,0,0]
	v_mfma_scale_f32_16x16x128_f8f6f4 v[192:195], v[26:33], v[42:49], v[192:195], v216, v216 op_sel_hi:[0,0,0]
	v_mfma_scale_f32_16x16x128_f8f6f4 v[188:191], v[18:25], v[50:57], v[188:191], v216, v216 op_sel_hi:[0,0,0]
	v_mfma_scale_f32_16x16x128_f8f6f4 v[184:187], v[26:33], v[50:57], v[184:187], v216, v216 op_sel_hi:[0,0,0]
	v_mfma_scale_f32_16x16x128_f8f6f4 v[180:183], v[18:25], v[58:65], v[180:183], v216, v216 op_sel_hi:[0,0,0]
	v_mfma_scale_f32_16x16x128_f8f6f4 v[176:179], v[26:33], v[58:65], v[176:179], v216, v216 op_sel_hi:[0,0,0]
	v_mfma_scale_f32_16x16x128_f8f6f4 v[172:175], v[18:25], v[240:247], v[172:175], v216, v216 op_sel_hi:[0,0,0]
	v_mfma_scale_f32_16x16x128_f8f6f4 v[168:171], v[26:33], v[240:247], v[168:171], v216, v216 op_sel_hi:[0,0,0]
	s_setprio 0
	s_barrier
	s_mov_b32 m0, s58
	v_lshl_add_u64 v[34:35], v[34:35], 0, s[22:23]
	s_add_u32 s40, s40, 0x40080
	ds_read_b128 v[42:45], v219 offset:49152
	ds_read_b128 v[46:49], v219 offset:50176
	ds_read_b128 v[50:53], v219 offset:51200
	ds_read_b128 v[54:57], v219 offset:52224
	ds_read_b128 v[58:61], v219 offset:53248
	ds_read_b128 v[62:65], v219 offset:54272
	ds_read_b128 v[240:243], v219 offset:55296
	ds_read_b128 v[244:247], v219 offset:56320
	global_load_lds_dwordx4 v[34:35], off
	v_lshl_add_u64 v[34:35], v[36:37], 0, s[22:23]
	s_mov_b32 m0, s59
	s_addc_u32 s41, s41, 0
	global_load_lds_dwordx4 v[34:35], off
	v_lshl_add_u64 v[34:35], s[40:41], 0, v[200:201]
	s_mov_b32 m0, s62
	s_nop 0
	global_load_lds_dwordx4 v[34:35], off
	v_lshl_add_u64 v[34:35], s[40:41], 0, v[202:203]
	s_mov_b32 m0, s63
	s_nop 0
	global_load_lds_dwordx4 v[34:35], off
	v_lshl_add_u64 v[34:35], v[40:41], 0, s[22:23]
	s_mov_b32 m0, s60
	s_nop 0
	global_load_lds_dwordx4 v[34:35], off
	v_lshl_add_u64 v[34:35], v[38:39], 0, s[22:23]
	s_mov_b32 m0, s61
	s_nop 0
	global_load_lds_dwordx4 v[34:35], off
	s_waitcnt vmcnt(8)
	s_waitcnt lgkmcnt(0)
	s_barrier
	s_setprio 1
	s_waitcnt lgkmcnt(0)
	v_mfma_scale_f32_16x16x128_f8f6f4 v[100:103], v[2:9], v[42:49], v[100:103], v216, v216 op_sel_hi:[0,0,0]
	v_mfma_scale_f32_16x16x128_f8f6f4 v[96:99], v[10:17], v[42:49], v[96:99], v216, v216 op_sel_hi:[0,0,0]
	v_mfma_scale_f32_16x16x128_f8f6f4 v[92:95], v[2:9], v[50:57], v[92:95], v216, v216 op_sel_hi:[0,0,0]
	v_mfma_scale_f32_16x16x128_f8f6f4 v[88:91], v[10:17], v[50:57], v[88:91], v216, v216 op_sel_hi:[0,0,0]
	v_mfma_scale_f32_16x16x128_f8f6f4 v[84:87], v[2:9], v[58:65], v[84:87], v216, v216 op_sel_hi:[0,0,0]
	v_mfma_scale_f32_16x16x128_f8f6f4 v[80:83], v[10:17], v[58:65], v[80:83], v216, v216 op_sel_hi:[0,0,0]
	v_mfma_scale_f32_16x16x128_f8f6f4 v[76:79], v[2:9], v[240:247], v[76:79], v216, v216 op_sel_hi:[0,0,0]
	v_mfma_scale_f32_16x16x128_f8f6f4 v[72:75], v[10:17], v[240:247], v[72:75], v216, v216 op_sel_hi:[0,0,0]
	v_mfma_scale_f32_16x16x128_f8f6f4 v[164:167], v[18:25], v[42:49], v[164:167], v216, v216 op_sel_hi:[0,0,0]
	v_mfma_scale_f32_16x16x128_f8f6f4 v[160:163], v[26:33], v[42:49], v[160:163], v216, v216 op_sel_hi:[0,0,0]
	v_mfma_scale_f32_16x16x128_f8f6f4 v[148:151], v[18:25], v[50:57], v[148:151], v216, v216 op_sel_hi:[0,0,0]
	v_mfma_scale_f32_16x16x128_f8f6f4 v[136:139], v[26:33], v[50:57], v[136:139], v216, v216 op_sel_hi:[0,0,0]
	v_mfma_scale_f32_16x16x128_f8f6f4 v[156:159], v[18:25], v[58:65], v[156:159], v216, v216 op_sel_hi:[0,0,0]
	v_mfma_scale_f32_16x16x128_f8f6f4 v[152:155], v[26:33], v[58:65], v[152:155], v216, v216 op_sel_hi:[0,0,0]
	v_mfma_scale_f32_16x16x128_f8f6f4 v[144:147], v[18:25], v[240:247], v[144:147], v216, v216 op_sel_hi:[0,0,0]
	v_mfma_scale_f32_16x16x128_f8f6f4 v[140:143], v[26:33], v[240:247], v[140:143], v216, v216 op_sel_hi:[0,0,0]
	s_setprio 0
	s_barrier
	s_add_i32 s78, s78, 2
	s_add_u32 s38, s38, 0x100
	s_addc_u32 s39, s39, 0
	s_add_u32 s76, s76, 0x100
	s_addc_u32 s77, s77, 0
	s_cmp_gt_u32 s78, 13
	s_cbranch_scc1 .LBB0_219

.LBB0_472:
	s_waitcnt vmcnt(8)
	s_add_u32 s24, s20, 0x80
	s_waitcnt lgkmcnt(0)
	s_addc_u32 s25, s21, 0
	s_and_b64 s[22:23], s[22:23], exec
	s_cselect_b32 s25, s3, s25
	s_cselect_b32 s24, s2, s24
	s_cselect_b32 s23, s47, s51
	s_cselect_b32 s22, s49, s50
	s_barrier
	s_setprio 1
	s_waitcnt lgkmcnt(0)
	v_mfma_f32_16x16x32_bf16 v[148:151], v[152:155], v[192:195], v[148:151]
	v_mfma_f32_16x16x32_bf16 v[144:147], v[160:163], v[192:195], v[144:147]
	v_mfma_f32_16x16x32_bf16 v[132:135], v[152:155], v[184:187], v[132:135]
	v_mfma_f32_16x16x32_bf16 v[128:131], v[160:163], v[184:187], v[128:131]
	v_mfma_f32_16x16x32_bf16 v[116:119], v[152:155], v[176:179], v[116:119]
	v_mfma_f32_16x16x32_bf16 v[112:115], v[160:163], v[176:179], v[112:115]
	v_mfma_f32_16x16x32_bf16 v[84:87], v[152:155], v[168:171], v[84:87]
	v_mfma_f32_16x16x32_bf16 v[80:83], v[160:163], v[168:171], v[80:83]
	v_mfma_f32_16x16x32_bf16 v[148:151], v[156:159], v[196:199], v[148:151]
	v_mfma_f32_16x16x32_bf16 v[144:147], v[164:167], v[196:199], v[144:147]
	v_mfma_f32_16x16x32_bf16 v[132:135], v[156:159], v[188:191], v[132:135]
	v_mfma_f32_16x16x32_bf16 v[128:131], v[164:167], v[188:191], v[128:131]
	v_mfma_f32_16x16x32_bf16 v[116:119], v[156:159], v[180:183], v[116:119]
	v_mfma_f32_16x16x32_bf16 v[112:115], v[164:167], v[180:183], v[112:115]
	v_mfma_f32_16x16x32_bf16 v[84:87], v[156:159], v[172:175], v[84:87]
	v_mfma_f32_16x16x32_bf16 v[80:83], v[164:167], v[172:175], v[80:83]
	v_mfma_f32_16x16x32_bf16 v[140:143], v[88:91], v[192:195], v[140:143]
	v_mfma_f32_16x16x32_bf16 v[136:139], v[104:107], v[192:195], v[136:139]
	v_mfma_f32_16x16x32_bf16 v[124:127], v[88:91], v[184:187], v[124:127]
	v_mfma_f32_16x16x32_bf16 v[120:123], v[104:107], v[184:187], v[120:123]
	v_mfma_f32_16x16x32_bf16 v[100:103], v[88:91], v[176:179], v[100:103]
	v_mfma_f32_16x16x32_bf16 v[96:99], v[104:107], v[176:179], v[96:99]
	v_mfma_f32_16x16x32_bf16 v[76:79], v[88:91], v[168:171], v[76:79]
	v_mfma_f32_16x16x32_bf16 v[72:75], v[104:107], v[168:171], v[72:75]
	v_mfma_f32_16x16x32_bf16 v[140:143], v[92:95], v[196:199], v[140:143]
	v_mfma_f32_16x16x32_bf16 v[136:139], v[108:111], v[196:199], v[136:139]
	v_mfma_f32_16x16x32_bf16 v[124:127], v[92:95], v[188:191], v[124:127]
	v_mfma_f32_16x16x32_bf16 v[120:123], v[108:111], v[188:191], v[120:123]
	v_mfma_f32_16x16x32_bf16 v[100:103], v[92:95], v[180:183], v[100:103]
	v_mfma_f32_16x16x32_bf16 v[96:99], v[108:111], v[180:183], v[96:99]
	v_mfma_f32_16x16x32_bf16 v[76:79], v[92:95], v[172:175], v[76:79]
	v_mfma_f32_16x16x32_bf16 v[72:75], v[108:111], v[172:175], v[72:75]
	s_setprio 0
	s_barrier
	s_mov_b32 m0, s30
	v_lshl_add_u64 v[4:5], s[22:23], 0, v[202:203]
	s_add_u32 s54, s22, 0x20000
	ds_read_b128 v[168:171], v222 offset:16384
	ds_read_b128 v[172:175], v222 offset:17408
	ds_read_b128 v[176:179], v222 offset:18432
	ds_read_b128 v[180:183], v222 offset:19456
	ds_read_b128 v[184:187], v222 offset:20480
	ds_read_b128 v[188:191], v222 offset:21504
	ds_read_b128 v[192:195], v222 offset:22528
	ds_read_b128 v[196:199], v222 offset:23552
	global_load_lds_dwordx4 v[4:5], off
	v_lshl_add_u64 v[224:225], s[22:23], 0, v[200:201]
	s_mov_b32 m0, s31
	s_addc_u32 s55, s23, 0
	global_load_lds_dwordx4 v[224:225], off
	v_lshl_add_u64 v[226:227], s[54:55], 0, v[202:203]
	s_mov_b32 m0, s33
	v_mov_b32_e32 v205, v3
	global_load_lds_dwordx4 v[226:227], off
	v_lshl_add_u64 v[226:227], s[54:55], 0, v[200:201]
	s_mov_b32 m0, s34
	v_lshl_add_u64 v[228:229], s[24:25], 0, v[204:205]
	global_load_lds_dwordx4 v[226:227], off
	s_mov_b32 m0, s29
	v_lshl_add_u64 v[226:227], s[24:25], 0, v[2:3]
	global_load_lds_dwordx4 v2, s[24:25]
	s_mov_b32 m0, s35
	s_nop 0
	global_load_lds_dwordx4 v204, s[24:25]
	s_waitcnt vmcnt(8)
	s_waitcnt lgkmcnt(0)
	s_barrier
	s_setprio 1
	s_waitcnt lgkmcnt(0)
	v_mfma_f32_16x16x32_bf16 v[68:71], v[152:155], v[168:171], v[68:71]
	v_mfma_f32_16x16x32_bf16 v[64:67], v[160:163], v[168:171], v[64:67]
	v_mfma_f32_16x16x32_bf16 v[52:55], v[152:155], v[176:179], v[52:55]
	v_mfma_f32_16x16x32_bf16 v[48:51], v[160:163], v[176:179], v[48:51]
	v_mfma_f32_16x16x32_bf16 v[36:39], v[152:155], v[184:187], v[36:39]
	v_mfma_f32_16x16x32_bf16 v[24:27], v[160:163], v[184:187], v[24:27]
	v_mfma_f32_16x16x32_bf16 v[12:15], v[152:155], v[192:195], v[12:15]
	v_mfma_f32_16x16x32_bf16 v[8:11], v[160:163], v[192:195], v[8:11]
	v_mfma_f32_16x16x32_bf16 v[68:71], v[156:159], v[172:175], v[68:71]
	v_mfma_f32_16x16x32_bf16 v[64:67], v[164:167], v[172:175], v[64:67]
	v_mfma_f32_16x16x32_bf16 v[52:55], v[156:159], v[180:183], v[52:55]
	v_mfma_f32_16x16x32_bf16 v[48:51], v[164:167], v[180:183], v[48:51]
	v_mfma_f32_16x16x32_bf16 v[36:39], v[156:159], v[188:191], v[36:39]
	v_mfma_f32_16x16x32_bf16 v[24:27], v[164:167], v[188:191], v[24:27]
	v_mfma_f32_16x16x32_bf16 v[12:15], v[156:159], v[196:199], v[12:15]
	v_mfma_f32_16x16x32_bf16 v[8:11], v[164:167], v[196:199], v[8:11]
	v_mfma_f32_16x16x32_bf16 v[60:63], v[88:91], v[168:171], v[60:63]
	v_mfma_f32_16x16x32_bf16 v[56:59], v[104:107], v[168:171], v[56:59]
	v_mfma_f32_16x16x32_bf16 v[44:47], v[88:91], v[176:179], v[44:47]
	v_mfma_f32_16x16x32_bf16 v[40:43], v[104:107], v[176:179], v[40:43]
	v_mfma_f32_16x16x32_bf16 v[32:35], v[88:91], v[184:187], v[32:35]
	v_mfma_f32_16x16x32_bf16 v[28:31], v[104:107], v[184:187], v[28:31]
	v_mfma_f32_16x16x32_bf16 v[20:23], v[88:91], v[192:195], v[20:23]
	v_mfma_f32_16x16x32_bf16 v[16:19], v[104:107], v[192:195], v[16:19]
	v_mfma_f32_16x16x32_bf16 v[60:63], v[92:95], v[172:175], v[60:63]
	v_mfma_f32_16x16x32_bf16 v[56:59], v[108:111], v[172:175], v[56:59]
	v_mfma_f32_16x16x32_bf16 v[44:47], v[92:95], v[180:183], v[44:47]
	v_mfma_f32_16x16x32_bf16 v[40:43], v[108:111], v[180:183], v[40:43]
	v_mfma_f32_16x16x32_bf16 v[32:35], v[92:95], v[188:191], v[32:35]
	v_mfma_f32_16x16x32_bf16 v[28:31], v[108:111], v[188:191], v[28:31]
	v_mfma_f32_16x16x32_bf16 v[20:23], v[92:95], v[196:199], v[20:23]
	v_mfma_f32_16x16x32_bf16 v[16:19], v[108:111], v[196:199], v[16:19]
	s_setprio 0
	s_barrier
	s_add_i32 s53, 0, 0x18000
	v_add_u32_e32 v7, s53, v218
	s_add_i32 s54, 0, 0x1c000
	ds_read_b128 v[88:91], v7
	ds_read_b128 v[92:95], v7 offset:1024
	ds_read_b128 v[104:107], v7 offset:2048
	ds_read_b128 v[108:111], v7 offset:3072
	v_add_u32_e32 v7, s54, v218
	ds_read_b128 v[152:155], v7
	ds_read_b128 v[156:159], v7 offset:1024
	ds_read_b128 v[160:163], v7 offset:2048
	ds_read_b128 v[164:167], v7 offset:3072
	s_mov_b32 m0, s36
	v_lshl_add_u64 v[210:211], s[24:25], 0, v[210:211]
	ds_read_b128 v[168:171], v222 offset:32768
	ds_read_b128 v[172:175], v222 offset:33792
	ds_read_b128 v[176:179], v222 offset:34816
	ds_read_b128 v[180:183], v222 offset:35840
	ds_read_b128 v[184:187], v222 offset:36864
	ds_read_b128 v[188:191], v222 offset:37888
	ds_read_b128 v[192:195], v222 offset:38912
	ds_read_b128 v[196:199], v222 offset:39936
	global_load_lds_dwordx4 v[210:211], off
	v_lshl_add_u64 v[208:209], s[24:25], 0, v[208:209]
	s_mov_b32 m0, s37
	s_nop 0
	global_load_lds_dwordx4 v[208:209], off
	s_waitcnt vmcnt(8)
	s_waitcnt lgkmcnt(0)
	s_barrier
	s_setprio 1
	s_waitcnt lgkmcnt(0)
	v_mfma_f32_16x16x32_bf16 v[148:151], v[88:91], v[168:171], v[148:151]
	v_mfma_f32_16x16x32_bf16 v[144:147], v[104:107], v[168:171], v[144:147]
	v_mfma_f32_16x16x32_bf16 v[132:135], v[88:91], v[176:179], v[132:135]
	v_mfma_f32_16x16x32_bf16 v[128:131], v[104:107], v[176:179], v[128:131]
	v_mfma_f32_16x16x32_bf16 v[116:119], v[88:91], v[184:187], v[116:119]
	v_mfma_f32_16x16x32_bf16 v[112:115], v[104:107], v[184:187], v[112:115]
	v_mfma_f32_16x16x32_bf16 v[84:87], v[88:91], v[192:195], v[84:87]
	v_mfma_f32_16x16x32_bf16 v[80:83], v[104:107], v[192:195], v[80:83]
	v_mfma_f32_16x16x32_bf16 v[148:151], v[92:95], v[172:175], v[148:151]
	v_mfma_f32_16x16x32_bf16 v[144:147], v[108:111], v[172:175], v[144:147]
	v_mfma_f32_16x16x32_bf16 v[132:135], v[92:95], v[180:183], v[132:135]
	v_mfma_f32_16x16x32_bf16 v[128:131], v[108:111], v[180:183], v[128:131]
	v_mfma_f32_16x16x32_bf16 v[116:119], v[92:95], v[188:191], v[116:119]
	v_mfma_f32_16x16x32_bf16 v[112:115], v[108:111], v[188:191], v[112:115]
	v_mfma_f32_16x16x32_bf16 v[84:87], v[92:95], v[196:199], v[84:87]
	v_mfma_f32_16x16x32_bf16 v[80:83], v[108:111], v[196:199], v[80:83]
	v_mfma_f32_16x16x32_bf16 v[140:143], v[152:155], v[168:171], v[140:143]
	v_mfma_f32_16x16x32_bf16 v[136:139], v[160:163], v[168:171], v[136:139]
	v_mfma_f32_16x16x32_bf16 v[124:127], v[152:155], v[176:179], v[124:127]
	v_mfma_f32_16x16x32_bf16 v[120:123], v[160:163], v[176:179], v[120:123]
	v_mfma_f32_16x16x32_bf16 v[100:103], v[152:155], v[184:187], v[100:103]
	v_mfma_f32_16x16x32_bf16 v[96:99], v[160:163], v[184:187], v[96:99]
	v_mfma_f32_16x16x32_bf16 v[76:79], v[152:155], v[192:195], v[76:79]
	v_mfma_f32_16x16x32_bf16 v[72:75], v[160:163], v[192:195], v[72:75]
	v_mfma_f32_16x16x32_bf16 v[140:143], v[156:159], v[172:175], v[140:143]
	v_mfma_f32_16x16x32_bf16 v[136:139], v[164:167], v[172:175], v[136:139]
	v_mfma_f32_16x16x32_bf16 v[124:127], v[156:159], v[180:183], v[124:127]
	v_mfma_f32_16x16x32_bf16 v[120:123], v[164:167], v[180:183], v[120:123]
	v_mfma_f32_16x16x32_bf16 v[100:103], v[156:159], v[188:191], v[100:103]
	v_mfma_f32_16x16x32_bf16 v[96:99], v[164:167], v[188:191], v[96:99]
	v_mfma_f32_16x16x32_bf16 v[76:79], v[156:159], v[196:199], v[76:79]
	v_mfma_f32_16x16x32_bf16 v[72:75], v[164:167], v[196:199], v[72:75]
	s_setprio 0
	s_barrier
	s_add_i32 s24, s53, s28
	v_lshl_add_u64 v[4:5], v[4:5], 0, s[10:11]
	s_mov_b32 m0, s24
	ds_read_b128 v[168:171], v222 offset:49152
	ds_read_b128 v[172:175], v222 offset:50176
	ds_read_b128 v[176:179], v222 offset:51200
	ds_read_b128 v[180:183], v222 offset:52224
	ds_read_b128 v[184:187], v222 offset:53248
	ds_read_b128 v[188:191], v222 offset:54272
	ds_read_b128 v[192:195], v222 offset:55296
	ds_read_b128 v[196:199], v222 offset:56320
	global_load_lds_dwordx4 v[4:5], off
	s_add_i32 m0, s24, 0x2000
	s_add_u32 s22, s22, 0x20080
	v_lshl_add_u64 v[4:5], v[224:225], 0, s[10:11]
	s_addc_u32 s23, s23, 0
	s_add_i32 s24, s54, s28
	global_load_lds_dwordx4 v[4:5], off
	v_lshl_add_u64 v[4:5], s[22:23], 0, v[202:203]
	s_mov_b32 m0, s24
	s_nop 0
	global_load_lds_dwordx4 v[4:5], off
	v_lshl_add_u64 v[4:5], s[22:23], 0, v[200:201]
	s_add_i32 m0, s24, 0x2000
	s_nop 0
	global_load_lds_dwordx4 v[4:5], off
	v_lshl_add_u64 v[4:5], v[226:227], 0, s[10:11]
	s_mov_b32 m0, s39
	s_nop 0
	global_load_lds_dwordx4 v[4:5], off
	v_lshl_add_u64 v[4:5], v[228:229], 0, s[10:11]
	s_mov_b32 m0, s40
	s_nop 0
	global_load_lds_dwordx4 v[4:5], off
	s_waitcnt vmcnt(8)
	s_waitcnt lgkmcnt(0)
	s_barrier
	s_setprio 1
	s_waitcnt lgkmcnt(0)
	v_mfma_f32_16x16x32_bf16 v[68:71], v[88:91], v[168:171], v[68:71]
	v_mfma_f32_16x16x32_bf16 v[64:67], v[104:107], v[168:171], v[64:67]
	v_mfma_f32_16x16x32_bf16 v[52:55], v[88:91], v[176:179], v[52:55]
	v_mfma_f32_16x16x32_bf16 v[48:51], v[104:107], v[176:179], v[48:51]
	v_mfma_f32_16x16x32_bf16 v[36:39], v[88:91], v[184:187], v[36:39]
	v_mfma_f32_16x16x32_bf16 v[24:27], v[104:107], v[184:187], v[24:27]
	v_mfma_f32_16x16x32_bf16 v[12:15], v[88:91], v[192:195], v[12:15]
	v_mfma_f32_16x16x32_bf16 v[8:11], v[104:107], v[192:195], v[8:11]
	v_mfma_f32_16x16x32_bf16 v[68:71], v[92:95], v[172:175], v[68:71]
	v_mfma_f32_16x16x32_bf16 v[64:67], v[108:111], v[172:175], v[64:67]
	v_mfma_f32_16x16x32_bf16 v[52:55], v[92:95], v[180:183], v[52:55]
	v_mfma_f32_16x16x32_bf16 v[48:51], v[108:111], v[180:183], v[48:51]
	v_mfma_f32_16x16x32_bf16 v[36:39], v[92:95], v[188:191], v[36:39]
	v_mfma_f32_16x16x32_bf16 v[24:27], v[108:111], v[188:191], v[24:27]
	v_mfma_f32_16x16x32_bf16 v[12:15], v[92:95], v[196:199], v[12:15]
	v_mfma_f32_16x16x32_bf16 v[8:11], v[108:111], v[196:199], v[8:11]
	v_mfma_f32_16x16x32_bf16 v[60:63], v[152:155], v[168:171], v[60:63]
	v_mfma_f32_16x16x32_bf16 v[56:59], v[160:163], v[168:171], v[56:59]
	v_mfma_f32_16x16x32_bf16 v[44:47], v[152:155], v[176:179], v[44:47]
	v_mfma_f32_16x16x32_bf16 v[40:43], v[160:163], v[176:179], v[40:43]
	v_mfma_f32_16x16x32_bf16 v[32:35], v[152:155], v[184:187], v[32:35]
	v_mfma_f32_16x16x32_bf16 v[28:31], v[160:163], v[184:187], v[28:31]
	v_mfma_f32_16x16x32_bf16 v[20:23], v[152:155], v[192:195], v[20:23]
	v_mfma_f32_16x16x32_bf16 v[16:19], v[160:163], v[192:195], v[16:19]
	v_mfma_f32_16x16x32_bf16 v[60:63], v[156:159], v[172:175], v[60:63]
	v_mfma_f32_16x16x32_bf16 v[56:59], v[164:167], v[172:175], v[56:59]
	v_mfma_f32_16x16x32_bf16 v[44:47], v[156:159], v[180:183], v[44:47]
	v_mfma_f32_16x16x32_bf16 v[40:43], v[164:167], v[180:183], v[40:43]
	v_mfma_f32_16x16x32_bf16 v[32:35], v[156:159], v[188:191], v[32:35]
	v_mfma_f32_16x16x32_bf16 v[28:31], v[164:167], v[188:191], v[28:31]
	v_mfma_f32_16x16x32_bf16 v[20:23], v[156:159], v[196:199], v[20:23]
	v_mfma_f32_16x16x32_bf16 v[16:19], v[164:167], v[196:199], v[16:19]
	s_setprio 0
	s_barrier
	s_add_i32 s52, s52, 2
	s_add_u32 s20, s20, 0x100
	s_addc_u32 s21, s21, 0
	s_add_u32 s50, s50, 0x100
	s_addc_u32 s51, s51, 0
	s_cmp_gt_u32 s52, 5
	s_cbranch_scc1 .LBB0_475

.LBB0_675:
	s_waitcnt vmcnt(8)
	s_add_u32 s26, s22, 0x80
	s_waitcnt lgkmcnt(0)
	s_addc_u32 s27, s23, 0
	s_and_b64 s[24:25], s[24:25], exec
	s_cselect_b32 s27, s5, s27
	s_cselect_b32 s26, s4, s26
	s_cselect_b32 s25, s19, s50
	s_cselect_b32 s24, s48, s49
	s_barrier
	s_setprio 1
	s_waitcnt lgkmcnt(0)
	v_mfma_f32_16x16x32_bf16 v[132:135], v[152:155], v[192:195], v[132:135]
	v_mfma_f32_16x16x32_bf16 v[128:131], v[160:163], v[192:195], v[128:131]
	v_mfma_f32_16x16x32_bf16 v[116:119], v[152:155], v[184:187], v[116:119]
	v_mfma_f32_16x16x32_bf16 v[112:115], v[160:163], v[184:187], v[112:115]
	v_mfma_f32_16x16x32_bf16 v[100:103], v[152:155], v[176:179], v[100:103]
	v_mfma_f32_16x16x32_bf16 v[96:99], v[160:163], v[176:179], v[96:99]
	v_mfma_f32_16x16x32_bf16 v[84:87], v[152:155], v[168:171], v[84:87]
	v_mfma_f32_16x16x32_bf16 v[80:83], v[160:163], v[168:171], v[80:83]
	v_mfma_f32_16x16x32_bf16 v[132:135], v[156:159], v[196:199], v[132:135]
	v_mfma_f32_16x16x32_bf16 v[128:131], v[164:167], v[196:199], v[128:131]
	v_mfma_f32_16x16x32_bf16 v[116:119], v[156:159], v[188:191], v[116:119]
	v_mfma_f32_16x16x32_bf16 v[112:115], v[164:167], v[188:191], v[112:115]
	v_mfma_f32_16x16x32_bf16 v[100:103], v[156:159], v[180:183], v[100:103]
	v_mfma_f32_16x16x32_bf16 v[96:99], v[164:167], v[180:183], v[96:99]
	v_mfma_f32_16x16x32_bf16 v[84:87], v[156:159], v[172:175], v[84:87]
	v_mfma_f32_16x16x32_bf16 v[80:83], v[164:167], v[172:175], v[80:83]
	v_mfma_f32_16x16x32_bf16 v[124:127], v[136:139], v[192:195], v[124:127]
	v_mfma_f32_16x16x32_bf16 v[120:123], v[144:147], v[192:195], v[120:123]
	v_mfma_f32_16x16x32_bf16 v[108:111], v[136:139], v[184:187], v[108:111]
	v_mfma_f32_16x16x32_bf16 v[104:107], v[144:147], v[184:187], v[104:107]
	v_mfma_f32_16x16x32_bf16 v[92:95], v[136:139], v[176:179], v[92:95]
	v_mfma_f32_16x16x32_bf16 v[88:91], v[144:147], v[176:179], v[88:91]
	v_mfma_f32_16x16x32_bf16 v[76:79], v[136:139], v[168:171], v[76:79]
	v_mfma_f32_16x16x32_bf16 v[72:75], v[144:147], v[168:171], v[72:75]
	v_mfma_f32_16x16x32_bf16 v[124:127], v[140:143], v[196:199], v[124:127]
	v_mfma_f32_16x16x32_bf16 v[120:123], v[148:151], v[196:199], v[120:123]
	v_mfma_f32_16x16x32_bf16 v[108:111], v[140:143], v[188:191], v[108:111]
	v_mfma_f32_16x16x32_bf16 v[104:107], v[148:151], v[188:191], v[104:107]
	v_mfma_f32_16x16x32_bf16 v[92:95], v[140:143], v[180:183], v[92:95]
	v_mfma_f32_16x16x32_bf16 v[88:91], v[148:151], v[180:183], v[88:91]
	v_mfma_f32_16x16x32_bf16 v[76:79], v[140:143], v[172:175], v[76:79]
	v_mfma_f32_16x16x32_bf16 v[72:75], v[148:151], v[172:175], v[72:75]
	s_setprio 0
	s_barrier
	s_mov_b32 m0, s34
	v_lshl_add_u64 v[4:5], s[24:25], 0, v[200:201]
	s_add_u32 s52, s24, 0x100000
	ds_read_b128 v[168:171], v225 offset:16384
	ds_read_b128 v[172:175], v225 offset:17408
	ds_read_b128 v[176:179], v225 offset:18432
	ds_read_b128 v[180:183], v225 offset:19456
	ds_read_b128 v[184:187], v225 offset:20480
	ds_read_b128 v[188:191], v225 offset:21504
	ds_read_b128 v[192:195], v225 offset:22528
	ds_read_b128 v[196:199], v225 offset:23552
	global_load_lds_dwordx4 v[4:5], off
	v_lshl_add_u64 v[226:227], s[24:25], 0, v[202:203]
	s_mov_b32 m0, s35
	s_addc_u32 s53, s25, 0
	global_load_lds_dwordx4 v[226:227], off
	v_lshl_add_u64 v[228:229], s[52:53], 0, v[200:201]
	s_mov_b32 m0, s36
	v_mov_b32_e32 v205, v3
	global_load_lds_dwordx4 v[228:229], off
	v_lshl_add_u64 v[228:229], s[52:53], 0, v[202:203]
	s_mov_b32 m0, s37
	v_lshl_add_u64 v[230:231], s[26:27], 0, v[204:205]
	global_load_lds_dwordx4 v[228:229], off
	s_mov_b32 m0, s33
	v_lshl_add_u64 v[228:229], s[26:27], 0, v[2:3]
	global_load_lds_dwordx4 v2, s[26:27]
	s_mov_b32 m0, s38
	s_nop 0
	global_load_lds_dwordx4 v204, s[26:27]
	s_waitcnt vmcnt(8)
	s_waitcnt lgkmcnt(0)
	s_barrier
	s_setprio 1
	s_waitcnt lgkmcnt(0)
	v_mfma_f32_16x16x32_bf16 v[68:71], v[152:155], v[168:171], v[68:71]
	v_mfma_f32_16x16x32_bf16 v[64:67], v[160:163], v[168:171], v[64:67]
	v_mfma_f32_16x16x32_bf16 v[52:55], v[152:155], v[176:179], v[52:55]
	v_mfma_f32_16x16x32_bf16 v[48:51], v[160:163], v[176:179], v[48:51]
	v_mfma_f32_16x16x32_bf16 v[36:39], v[152:155], v[184:187], v[36:39]
	v_mfma_f32_16x16x32_bf16 v[28:31], v[160:163], v[184:187], v[28:31]
	v_mfma_f32_16x16x32_bf16 v[16:19], v[152:155], v[192:195], v[16:19]
	v_mfma_f32_16x16x32_bf16 v[8:11], v[160:163], v[192:195], v[8:11]
	v_mfma_f32_16x16x32_bf16 v[68:71], v[156:159], v[172:175], v[68:71]
	v_mfma_f32_16x16x32_bf16 v[64:67], v[164:167], v[172:175], v[64:67]
	v_mfma_f32_16x16x32_bf16 v[52:55], v[156:159], v[180:183], v[52:55]
	v_mfma_f32_16x16x32_bf16 v[48:51], v[164:167], v[180:183], v[48:51]
	v_mfma_f32_16x16x32_bf16 v[36:39], v[156:159], v[188:191], v[36:39]
	v_mfma_f32_16x16x32_bf16 v[28:31], v[164:167], v[188:191], v[28:31]
	v_mfma_f32_16x16x32_bf16 v[16:19], v[156:159], v[196:199], v[16:19]
	v_mfma_f32_16x16x32_bf16 v[8:11], v[164:167], v[196:199], v[8:11]
	v_mfma_f32_16x16x32_bf16 v[60:63], v[136:139], v[168:171], v[60:63]
	v_mfma_f32_16x16x32_bf16 v[56:59], v[144:147], v[168:171], v[56:59]
	v_mfma_f32_16x16x32_bf16 v[44:47], v[136:139], v[176:179], v[44:47]
	v_mfma_f32_16x16x32_bf16 v[40:43], v[144:147], v[176:179], v[40:43]
	v_mfma_f32_16x16x32_bf16 v[32:35], v[136:139], v[184:187], v[32:35]
	v_mfma_f32_16x16x32_bf16 v[24:27], v[144:147], v[184:187], v[24:27]
	v_mfma_f32_16x16x32_bf16 v[20:23], v[136:139], v[192:195], v[20:23]
	v_mfma_f32_16x16x32_bf16 v[12:15], v[144:147], v[192:195], v[12:15]
	v_mfma_f32_16x16x32_bf16 v[60:63], v[140:143], v[172:175], v[60:63]
	v_mfma_f32_16x16x32_bf16 v[56:59], v[148:151], v[172:175], v[56:59]
	v_mfma_f32_16x16x32_bf16 v[44:47], v[140:143], v[180:183], v[44:47]
	v_mfma_f32_16x16x32_bf16 v[40:43], v[148:151], v[180:183], v[40:43]
	v_mfma_f32_16x16x32_bf16 v[32:35], v[140:143], v[188:191], v[32:35]
	v_mfma_f32_16x16x32_bf16 v[24:27], v[148:151], v[188:191], v[24:27]
	v_mfma_f32_16x16x32_bf16 v[20:23], v[140:143], v[196:199], v[20:23]
	v_mfma_f32_16x16x32_bf16 v[12:15], v[148:151], v[196:199], v[12:15]
	s_setprio 0
	s_barrier
	s_add_i32 s52, 0, 0x18000
	v_add_u32_e32 v7, s52, v221
	s_add_i32 s53, 0, 0x1c000
	ds_read_b128 v[136:139], v7
	ds_read_b128 v[140:143], v7 offset:1024
	ds_read_b128 v[144:147], v7 offset:2048
	ds_read_b128 v[148:151], v7 offset:3072
	v_add_u32_e32 v7, s53, v221
	ds_read_b128 v[152:155], v7
	ds_read_b128 v[156:159], v7 offset:1024
	ds_read_b128 v[160:163], v7 offset:2048
	ds_read_b128 v[164:167], v7 offset:3072
	s_mov_b32 m0, s39
	v_lshl_add_u64 v[214:215], s[26:27], 0, v[214:215]
	ds_read_b128 v[168:171], v225 offset:32768
	ds_read_b128 v[172:175], v225 offset:33792
	ds_read_b128 v[176:179], v225 offset:34816
	ds_read_b128 v[180:183], v225 offset:35840
	ds_read_b128 v[184:187], v225 offset:36864
	ds_read_b128 v[188:191], v225 offset:37888
	ds_read_b128 v[192:195], v225 offset:38912
	ds_read_b128 v[196:199], v225 offset:39936
	global_load_lds_dwordx4 v[214:215], off
	v_lshl_add_u64 v[212:213], s[26:27], 0, v[212:213]
	s_mov_b32 m0, s40
	s_nop 0
	global_load_lds_dwordx4 v[212:213], off
	s_waitcnt vmcnt(8)
	s_waitcnt lgkmcnt(0)
	s_barrier
	s_setprio 1
	s_waitcnt lgkmcnt(0)
	v_mfma_f32_16x16x32_bf16 v[132:135], v[136:139], v[168:171], v[132:135]
	v_mfma_f32_16x16x32_bf16 v[128:131], v[144:147], v[168:171], v[128:131]
	v_mfma_f32_16x16x32_bf16 v[116:119], v[136:139], v[176:179], v[116:119]
	v_mfma_f32_16x16x32_bf16 v[112:115], v[144:147], v[176:179], v[112:115]
	v_mfma_f32_16x16x32_bf16 v[100:103], v[136:139], v[184:187], v[100:103]
	v_mfma_f32_16x16x32_bf16 v[96:99], v[144:147], v[184:187], v[96:99]
	v_mfma_f32_16x16x32_bf16 v[84:87], v[136:139], v[192:195], v[84:87]
	v_mfma_f32_16x16x32_bf16 v[80:83], v[144:147], v[192:195], v[80:83]
	v_mfma_f32_16x16x32_bf16 v[132:135], v[140:143], v[172:175], v[132:135]
	v_mfma_f32_16x16x32_bf16 v[128:131], v[148:151], v[172:175], v[128:131]
	v_mfma_f32_16x16x32_bf16 v[116:119], v[140:143], v[180:183], v[116:119]
	v_mfma_f32_16x16x32_bf16 v[112:115], v[148:151], v[180:183], v[112:115]
	v_mfma_f32_16x16x32_bf16 v[100:103], v[140:143], v[188:191], v[100:103]
	v_mfma_f32_16x16x32_bf16 v[96:99], v[148:151], v[188:191], v[96:99]
	v_mfma_f32_16x16x32_bf16 v[84:87], v[140:143], v[196:199], v[84:87]
	v_mfma_f32_16x16x32_bf16 v[80:83], v[148:151], v[196:199], v[80:83]
	v_mfma_f32_16x16x32_bf16 v[124:127], v[152:155], v[168:171], v[124:127]
	v_mfma_f32_16x16x32_bf16 v[120:123], v[160:163], v[168:171], v[120:123]
	v_mfma_f32_16x16x32_bf16 v[108:111], v[152:155], v[176:179], v[108:111]
	v_mfma_f32_16x16x32_bf16 v[104:107], v[160:163], v[176:179], v[104:107]
	v_mfma_f32_16x16x32_bf16 v[92:95], v[152:155], v[184:187], v[92:95]
	v_mfma_f32_16x16x32_bf16 v[88:91], v[160:163], v[184:187], v[88:91]
	v_mfma_f32_16x16x32_bf16 v[76:79], v[152:155], v[192:195], v[76:79]
	v_mfma_f32_16x16x32_bf16 v[72:75], v[160:163], v[192:195], v[72:75]
	v_mfma_f32_16x16x32_bf16 v[124:127], v[156:159], v[172:175], v[124:127]
	v_mfma_f32_16x16x32_bf16 v[120:123], v[164:167], v[172:175], v[120:123]
	v_mfma_f32_16x16x32_bf16 v[108:111], v[156:159], v[180:183], v[108:111]
	v_mfma_f32_16x16x32_bf16 v[104:107], v[164:167], v[180:183], v[104:107]
	v_mfma_f32_16x16x32_bf16 v[92:95], v[156:159], v[188:191], v[92:95]
	v_mfma_f32_16x16x32_bf16 v[88:91], v[164:167], v[188:191], v[88:91]
	v_mfma_f32_16x16x32_bf16 v[76:79], v[156:159], v[196:199], v[76:79]
	v_mfma_f32_16x16x32_bf16 v[72:75], v[164:167], v[196:199], v[72:75]
	s_setprio 0
	s_barrier
	s_add_i32 s26, s52, s31
	v_lshl_add_u64 v[4:5], v[4:5], 0, s[12:13]
	s_mov_b32 m0, s26
	ds_read_b128 v[168:171], v225 offset:49152
	ds_read_b128 v[172:175], v225 offset:50176
	ds_read_b128 v[176:179], v225 offset:51200
	ds_read_b128 v[180:183], v225 offset:52224
	ds_read_b128 v[184:187], v225 offset:53248
	ds_read_b128 v[188:191], v225 offset:54272
	ds_read_b128 v[192:195], v225 offset:55296
	ds_read_b128 v[196:199], v225 offset:56320
	global_load_lds_dwordx4 v[4:5], off
	s_add_i32 m0, s26, 0x2000
	s_add_u32 s24, s24, 0x100080
	v_lshl_add_u64 v[4:5], v[226:227], 0, s[12:13]
	s_addc_u32 s25, s25, 0
	s_add_i32 s26, s53, s31
	global_load_lds_dwordx4 v[4:5], off
	v_lshl_add_u64 v[4:5], s[24:25], 0, v[200:201]
	s_mov_b32 m0, s26
	s_nop 0
	global_load_lds_dwordx4 v[4:5], off
	v_lshl_add_u64 v[4:5], s[24:25], 0, v[202:203]
	s_add_i32 m0, s26, 0x2000
	s_nop 0
	global_load_lds_dwordx4 v[4:5], off
	v_lshl_add_u64 v[4:5], v[228:229], 0, s[12:13]
	s_mov_b32 m0, s42
	s_nop 0
	global_load_lds_dwordx4 v[4:5], off
	v_lshl_add_u64 v[4:5], v[230:231], 0, s[12:13]
	s_mov_b32 m0, s43
	s_nop 0
	global_load_lds_dwordx4 v[4:5], off
	s_waitcnt vmcnt(8)
	s_waitcnt lgkmcnt(0)
	s_barrier
	s_setprio 1
	s_waitcnt lgkmcnt(0)
	v_mfma_f32_16x16x32_bf16 v[68:71], v[136:139], v[168:171], v[68:71]
	v_mfma_f32_16x16x32_bf16 v[64:67], v[144:147], v[168:171], v[64:67]
	v_mfma_f32_16x16x32_bf16 v[52:55], v[136:139], v[176:179], v[52:55]
	v_mfma_f32_16x16x32_bf16 v[48:51], v[144:147], v[176:179], v[48:51]
	v_mfma_f32_16x16x32_bf16 v[36:39], v[136:139], v[184:187], v[36:39]
	v_mfma_f32_16x16x32_bf16 v[28:31], v[144:147], v[184:187], v[28:31]
	v_mfma_f32_16x16x32_bf16 v[16:19], v[136:139], v[192:195], v[16:19]
	v_mfma_f32_16x16x32_bf16 v[8:11], v[144:147], v[192:195], v[8:11]
	v_mfma_f32_16x16x32_bf16 v[68:71], v[140:143], v[172:175], v[68:71]
	v_mfma_f32_16x16x32_bf16 v[64:67], v[148:151], v[172:175], v[64:67]
	v_mfma_f32_16x16x32_bf16 v[52:55], v[140:143], v[180:183], v[52:55]
	v_mfma_f32_16x16x32_bf16 v[48:51], v[148:151], v[180:183], v[48:51]
	v_mfma_f32_16x16x32_bf16 v[36:39], v[140:143], v[188:191], v[36:39]
	v_mfma_f32_16x16x32_bf16 v[28:31], v[148:151], v[188:191], v[28:31]
	v_mfma_f32_16x16x32_bf16 v[16:19], v[140:143], v[196:199], v[16:19]
	v_mfma_f32_16x16x32_bf16 v[8:11], v[148:151], v[196:199], v[8:11]
	v_mfma_f32_16x16x32_bf16 v[60:63], v[152:155], v[168:171], v[60:63]
	v_mfma_f32_16x16x32_bf16 v[56:59], v[160:163], v[168:171], v[56:59]
	v_mfma_f32_16x16x32_bf16 v[44:47], v[152:155], v[176:179], v[44:47]
	v_mfma_f32_16x16x32_bf16 v[40:43], v[160:163], v[176:179], v[40:43]
	v_mfma_f32_16x16x32_bf16 v[32:35], v[152:155], v[184:187], v[32:35]
	v_mfma_f32_16x16x32_bf16 v[24:27], v[160:163], v[184:187], v[24:27]
	v_mfma_f32_16x16x32_bf16 v[20:23], v[152:155], v[192:195], v[20:23]
	v_mfma_f32_16x16x32_bf16 v[12:15], v[160:163], v[192:195], v[12:15]
	v_mfma_f32_16x16x32_bf16 v[60:63], v[156:159], v[172:175], v[60:63]
	v_mfma_f32_16x16x32_bf16 v[56:59], v[164:167], v[172:175], v[56:59]
	v_mfma_f32_16x16x32_bf16 v[44:47], v[156:159], v[180:183], v[44:47]
	v_mfma_f32_16x16x32_bf16 v[40:43], v[164:167], v[180:183], v[40:43]
	v_mfma_f32_16x16x32_bf16 v[32:35], v[156:159], v[188:191], v[32:35]
	v_mfma_f32_16x16x32_bf16 v[24:27], v[164:167], v[188:191], v[24:27]
	v_mfma_f32_16x16x32_bf16 v[20:23], v[156:159], v[196:199], v[20:23]
	v_mfma_f32_16x16x32_bf16 v[12:15], v[164:167], v[196:199], v[12:15]
	s_setprio 0
	s_barrier
	s_add_i32 s51, s51, 2
	s_add_u32 s22, s22, 0x100
	s_addc_u32 s23, s23, 0
	s_add_u32 s49, s49, 0x100
	s_addc_u32 s50, s50, 0
	s_cmp_gt_u32 s51, 61
	s_cbranch_scc1 .LBB0_678

.LBB0_759:
	s_waitcnt vmcnt(8)
	s_add_u32 s24, s20, 0x80
	s_waitcnt lgkmcnt(0)
	s_addc_u32 s25, s21, 0
	s_and_b64 s[22:23], s[22:23], exec
	s_cselect_b32 s25, s5, s25
	s_cselect_b32 s24, s4, s24
	s_cselect_b32 s23, s17, s48
	s_cselect_b32 s22, s46, s47
	s_barrier
	s_setprio 1
	s_waitcnt lgkmcnt(0)
	v_mfma_f32_16x16x32_bf16 v[132:135], v[152:155], v[192:195], v[132:135]
	v_mfma_f32_16x16x32_bf16 v[128:131], v[160:163], v[192:195], v[128:131]
	v_mfma_f32_16x16x32_bf16 v[124:127], v[152:155], v[184:187], v[124:127]
	v_mfma_f32_16x16x32_bf16 v[120:123], v[160:163], v[184:187], v[120:123]
	v_mfma_f32_16x16x32_bf16 v[116:119], v[152:155], v[176:179], v[116:119]
	v_mfma_f32_16x16x32_bf16 v[108:111], v[160:163], v[176:179], v[108:111]
	v_mfma_f32_16x16x32_bf16 v[88:91], v[152:155], v[168:171], v[88:91]
	v_mfma_f32_16x16x32_bf16 v[80:83], v[160:163], v[168:171], v[80:83]
	v_mfma_f32_16x16x32_bf16 v[132:135], v[156:159], v[196:199], v[132:135]
	v_mfma_f32_16x16x32_bf16 v[128:131], v[164:167], v[196:199], v[128:131]
	v_mfma_f32_16x16x32_bf16 v[124:127], v[156:159], v[188:191], v[124:127]
	v_mfma_f32_16x16x32_bf16 v[120:123], v[164:167], v[188:191], v[120:123]
	v_mfma_f32_16x16x32_bf16 v[116:119], v[156:159], v[180:183], v[116:119]
	v_mfma_f32_16x16x32_bf16 v[108:111], v[164:167], v[180:183], v[108:111]
	v_mfma_f32_16x16x32_bf16 v[88:91], v[156:159], v[172:175], v[88:91]
	v_mfma_f32_16x16x32_bf16 v[80:83], v[164:167], v[172:175], v[80:83]
	v_mfma_f32_16x16x32_bf16 v[112:115], v[136:139], v[192:195], v[112:115]
	v_mfma_f32_16x16x32_bf16 v[104:107], v[144:147], v[192:195], v[104:107]
	v_mfma_f32_16x16x32_bf16 v[100:103], v[136:139], v[184:187], v[100:103]
	v_mfma_f32_16x16x32_bf16 v[96:99], v[144:147], v[184:187], v[96:99]
	v_mfma_f32_16x16x32_bf16 v[92:95], v[136:139], v[176:179], v[92:95]
	v_mfma_f32_16x16x32_bf16 v[84:87], v[144:147], v[176:179], v[84:87]
	v_mfma_f32_16x16x32_bf16 v[76:79], v[136:139], v[168:171], v[76:79]
	v_mfma_f32_16x16x32_bf16 v[72:75], v[144:147], v[168:171], v[72:75]
	v_mfma_f32_16x16x32_bf16 v[112:115], v[140:143], v[196:199], v[112:115]
	v_mfma_f32_16x16x32_bf16 v[104:107], v[148:151], v[196:199], v[104:107]
	v_mfma_f32_16x16x32_bf16 v[100:103], v[140:143], v[188:191], v[100:103]
	v_mfma_f32_16x16x32_bf16 v[96:99], v[148:151], v[188:191], v[96:99]
	v_mfma_f32_16x16x32_bf16 v[92:95], v[140:143], v[180:183], v[92:95]
	v_mfma_f32_16x16x32_bf16 v[84:87], v[148:151], v[180:183], v[84:87]
	v_mfma_f32_16x16x32_bf16 v[76:79], v[140:143], v[172:175], v[76:79]
	v_mfma_f32_16x16x32_bf16 v[72:75], v[148:151], v[172:175], v[72:75]
	s_setprio 0
	s_barrier
	s_mov_b32 m0, s31
	v_lshl_add_u64 v[4:5], s[22:23], 0, v[200:201]
	s_add_u32 s50, s22, 0x80000
	ds_read_b128 v[168:171], v225 offset:16384
	ds_read_b128 v[172:175], v225 offset:17408
	ds_read_b128 v[176:179], v225 offset:18432
	ds_read_b128 v[180:183], v225 offset:19456
	ds_read_b128 v[184:187], v225 offset:20480
	ds_read_b128 v[188:191], v225 offset:21504
	ds_read_b128 v[192:195], v225 offset:22528
	ds_read_b128 v[196:199], v225 offset:23552
	global_load_lds_dwordx4 v[4:5], off
	v_lshl_add_u64 v[226:227], s[22:23], 0, v[202:203]
	s_mov_b32 m0, s33
	s_addc_u32 s51, s23, 0
	global_load_lds_dwordx4 v[226:227], off
	v_lshl_add_u64 v[228:229], s[50:51], 0, v[200:201]
	s_mov_b32 m0, s34
	v_mov_b32_e32 v205, v3
	global_load_lds_dwordx4 v[228:229], off
	v_lshl_add_u64 v[228:229], s[50:51], 0, v[202:203]
	s_mov_b32 m0, s35
	v_lshl_add_u64 v[230:231], s[24:25], 0, v[204:205]
	global_load_lds_dwordx4 v[228:229], off
	s_mov_b32 m0, s30
	v_lshl_add_u64 v[228:229], s[24:25], 0, v[2:3]
	global_load_lds_dwordx4 v2, s[24:25]
	s_mov_b32 m0, s36
	s_nop 0
	global_load_lds_dwordx4 v204, s[24:25]
	s_waitcnt vmcnt(8)
	s_waitcnt lgkmcnt(0)
	s_barrier
	s_setprio 1
	s_waitcnt lgkmcnt(0)
	v_mfma_f32_16x16x32_bf16 v[68:71], v[152:155], v[168:171], v[68:71]
	v_mfma_f32_16x16x32_bf16 v[64:67], v[160:163], v[168:171], v[64:67]
	v_mfma_f32_16x16x32_bf16 v[60:63], v[152:155], v[176:179], v[60:63]
	v_mfma_f32_16x16x32_bf16 v[56:59], v[160:163], v[176:179], v[56:59]
	v_mfma_f32_16x16x32_bf16 v[28:31], v[152:155], v[184:187], v[28:31]
	v_mfma_f32_16x16x32_bf16 v[20:23], v[160:163], v[184:187], v[20:23]
	v_mfma_f32_16x16x32_bf16 v[12:15], v[152:155], v[192:195], v[12:15]
	v_mfma_f32_16x16x32_bf16 v[8:11], v[160:163], v[192:195], v[8:11]
	v_mfma_f32_16x16x32_bf16 v[68:71], v[156:159], v[172:175], v[68:71]
	v_mfma_f32_16x16x32_bf16 v[64:67], v[164:167], v[172:175], v[64:67]
	v_mfma_f32_16x16x32_bf16 v[60:63], v[156:159], v[180:183], v[60:63]
	v_mfma_f32_16x16x32_bf16 v[56:59], v[164:167], v[180:183], v[56:59]
	v_mfma_f32_16x16x32_bf16 v[28:31], v[156:159], v[188:191], v[28:31]
	v_mfma_f32_16x16x32_bf16 v[20:23], v[164:167], v[188:191], v[20:23]
	v_mfma_f32_16x16x32_bf16 v[12:15], v[156:159], v[196:199], v[12:15]
	v_mfma_f32_16x16x32_bf16 v[8:11], v[164:167], v[196:199], v[8:11]
	v_mfma_f32_16x16x32_bf16 v[52:55], v[136:139], v[168:171], v[52:55]
	v_mfma_f32_16x16x32_bf16 v[48:51], v[144:147], v[168:171], v[48:51]
	v_mfma_f32_16x16x32_bf16 v[36:39], v[136:139], v[176:179], v[36:39]
	v_mfma_f32_16x16x32_bf16 v[16:19], v[144:147], v[176:179], v[16:19]
	v_mfma_f32_16x16x32_bf16 v[44:47], v[136:139], v[184:187], v[44:47]
	v_mfma_f32_16x16x32_bf16 v[40:43], v[144:147], v[184:187], v[40:43]
	v_mfma_f32_16x16x32_bf16 v[32:35], v[136:139], v[192:195], v[32:35]
	v_mfma_f32_16x16x32_bf16 v[24:27], v[144:147], v[192:195], v[24:27]
	v_mfma_f32_16x16x32_bf16 v[52:55], v[140:143], v[172:175], v[52:55]
	v_mfma_f32_16x16x32_bf16 v[48:51], v[148:151], v[172:175], v[48:51]
	v_mfma_f32_16x16x32_bf16 v[36:39], v[140:143], v[180:183], v[36:39]
	v_mfma_f32_16x16x32_bf16 v[16:19], v[148:151], v[180:183], v[16:19]
	v_mfma_f32_16x16x32_bf16 v[44:47], v[140:143], v[188:191], v[44:47]
	v_mfma_f32_16x16x32_bf16 v[40:43], v[148:151], v[188:191], v[40:43]
	v_mfma_f32_16x16x32_bf16 v[32:35], v[140:143], v[196:199], v[32:35]
	v_mfma_f32_16x16x32_bf16 v[24:27], v[148:151], v[196:199], v[24:27]
	s_setprio 0
	s_barrier
	s_add_i32 s50, 0, 0x18000
	v_add_u32_e32 v7, s50, v221
	s_add_i32 s51, 0, 0x1c000
	ds_read_b128 v[136:139], v7
	ds_read_b128 v[140:143], v7 offset:1024
	ds_read_b128 v[144:147], v7 offset:2048
	ds_read_b128 v[148:151], v7 offset:3072
	v_add_u32_e32 v7, s51, v221
	ds_read_b128 v[152:155], v7
	ds_read_b128 v[156:159], v7 offset:1024
	ds_read_b128 v[160:163], v7 offset:2048
	ds_read_b128 v[164:167], v7 offset:3072
	s_mov_b32 m0, s37
	v_lshl_add_u64 v[214:215], s[24:25], 0, v[214:215]
	ds_read_b128 v[168:171], v225 offset:32768
	ds_read_b128 v[172:175], v225 offset:33792
	ds_read_b128 v[176:179], v225 offset:34816
	ds_read_b128 v[180:183], v225 offset:35840
	ds_read_b128 v[184:187], v225 offset:36864
	ds_read_b128 v[188:191], v225 offset:37888
	ds_read_b128 v[192:195], v225 offset:38912
	ds_read_b128 v[196:199], v225 offset:39936
	global_load_lds_dwordx4 v[214:215], off
	v_lshl_add_u64 v[212:213], s[24:25], 0, v[212:213]
	s_mov_b32 m0, s38
	s_nop 0
	global_load_lds_dwordx4 v[212:213], off
	s_waitcnt vmcnt(8)
	s_waitcnt lgkmcnt(0)
	s_barrier
	s_setprio 1
	s_waitcnt lgkmcnt(0)
	v_mfma_f32_16x16x32_bf16 v[132:135], v[136:139], v[168:171], v[132:135]
	v_mfma_f32_16x16x32_bf16 v[128:131], v[144:147], v[168:171], v[128:131]
	v_mfma_f32_16x16x32_bf16 v[124:127], v[136:139], v[176:179], v[124:127]
	v_mfma_f32_16x16x32_bf16 v[120:123], v[144:147], v[176:179], v[120:123]
	v_mfma_f32_16x16x32_bf16 v[116:119], v[136:139], v[184:187], v[116:119]
	v_mfma_f32_16x16x32_bf16 v[108:111], v[144:147], v[184:187], v[108:111]
	v_mfma_f32_16x16x32_bf16 v[88:91], v[136:139], v[192:195], v[88:91]
	v_mfma_f32_16x16x32_bf16 v[80:83], v[144:147], v[192:195], v[80:83]
	v_mfma_f32_16x16x32_bf16 v[132:135], v[140:143], v[172:175], v[132:135]
	v_mfma_f32_16x16x32_bf16 v[128:131], v[148:151], v[172:175], v[128:131]
	v_mfma_f32_16x16x32_bf16 v[124:127], v[140:143], v[180:183], v[124:127]
	v_mfma_f32_16x16x32_bf16 v[120:123], v[148:151], v[180:183], v[120:123]
	v_mfma_f32_16x16x32_bf16 v[116:119], v[140:143], v[188:191], v[116:119]
	v_mfma_f32_16x16x32_bf16 v[108:111], v[148:151], v[188:191], v[108:111]
	v_mfma_f32_16x16x32_bf16 v[88:91], v[140:143], v[196:199], v[88:91]
	v_mfma_f32_16x16x32_bf16 v[80:83], v[148:151], v[196:199], v[80:83]
	v_mfma_f32_16x16x32_bf16 v[112:115], v[152:155], v[168:171], v[112:115]
	v_mfma_f32_16x16x32_bf16 v[104:107], v[160:163], v[168:171], v[104:107]
	v_mfma_f32_16x16x32_bf16 v[100:103], v[152:155], v[176:179], v[100:103]
	v_mfma_f32_16x16x32_bf16 v[96:99], v[160:163], v[176:179], v[96:99]
	v_mfma_f32_16x16x32_bf16 v[92:95], v[152:155], v[184:187], v[92:95]
	v_mfma_f32_16x16x32_bf16 v[84:87], v[160:163], v[184:187], v[84:87]
	v_mfma_f32_16x16x32_bf16 v[76:79], v[152:155], v[192:195], v[76:79]
	v_mfma_f32_16x16x32_bf16 v[72:75], v[160:163], v[192:195], v[72:75]
	v_mfma_f32_16x16x32_bf16 v[112:115], v[156:159], v[172:175], v[112:115]
	v_mfma_f32_16x16x32_bf16 v[104:107], v[164:167], v[172:175], v[104:107]
	v_mfma_f32_16x16x32_bf16 v[100:103], v[156:159], v[180:183], v[100:103]
	v_mfma_f32_16x16x32_bf16 v[96:99], v[164:167], v[180:183], v[96:99]
	v_mfma_f32_16x16x32_bf16 v[92:95], v[156:159], v[188:191], v[92:95]
	v_mfma_f32_16x16x32_bf16 v[84:87], v[164:167], v[188:191], v[84:87]
	v_mfma_f32_16x16x32_bf16 v[76:79], v[156:159], v[196:199], v[76:79]
	v_mfma_f32_16x16x32_bf16 v[72:75], v[164:167], v[196:199], v[72:75]
	s_setprio 0
	s_barrier
	s_add_i32 s24, s50, s29
	v_lshl_add_u64 v[4:5], v[4:5], 0, s[10:11]
	s_mov_b32 m0, s24
	ds_read_b128 v[168:171], v225 offset:49152
	ds_read_b128 v[172:175], v225 offset:50176
	ds_read_b128 v[176:179], v225 offset:51200
	ds_read_b128 v[180:183], v225 offset:52224
	ds_read_b128 v[184:187], v225 offset:53248
	ds_read_b128 v[188:191], v225 offset:54272
	ds_read_b128 v[192:195], v225 offset:55296
	ds_read_b128 v[196:199], v225 offset:56320
	global_load_lds_dwordx4 v[4:5], off
	s_add_i32 m0, s24, 0x2000
	s_add_u32 s22, s22, 0x80080
	v_lshl_add_u64 v[4:5], v[226:227], 0, s[10:11]
	s_addc_u32 s23, s23, 0
	s_add_i32 s24, s51, s29
	global_load_lds_dwordx4 v[4:5], off
	v_lshl_add_u64 v[4:5], s[22:23], 0, v[200:201]
	s_mov_b32 m0, s24
	s_nop 0
	global_load_lds_dwordx4 v[4:5], off
	v_lshl_add_u64 v[4:5], s[22:23], 0, v[202:203]
	s_add_i32 m0, s24, 0x2000
	s_nop 0
	global_load_lds_dwordx4 v[4:5], off
	v_lshl_add_u64 v[4:5], v[228:229], 0, s[10:11]
	s_mov_b32 m0, s40
	s_nop 0
	global_load_lds_dwordx4 v[4:5], off
	v_lshl_add_u64 v[4:5], v[230:231], 0, s[10:11]
	s_mov_b32 m0, s41
	s_nop 0
	global_load_lds_dwordx4 v[4:5], off
	s_waitcnt vmcnt(8)
	s_waitcnt lgkmcnt(0)
	s_barrier
	s_setprio 1
	s_waitcnt lgkmcnt(0)
	v_mfma_f32_16x16x32_bf16 v[68:71], v[136:139], v[168:171], v[68:71]
	v_mfma_f32_16x16x32_bf16 v[64:67], v[144:147], v[168:171], v[64:67]
	v_mfma_f32_16x16x32_bf16 v[60:63], v[136:139], v[176:179], v[60:63]
	v_mfma_f32_16x16x32_bf16 v[56:59], v[144:147], v[176:179], v[56:59]
	v_mfma_f32_16x16x32_bf16 v[28:31], v[136:139], v[184:187], v[28:31]
	v_mfma_f32_16x16x32_bf16 v[20:23], v[144:147], v[184:187], v[20:23]
	v_mfma_f32_16x16x32_bf16 v[12:15], v[136:139], v[192:195], v[12:15]
	v_mfma_f32_16x16x32_bf16 v[8:11], v[144:147], v[192:195], v[8:11]
	v_mfma_f32_16x16x32_bf16 v[68:71], v[140:143], v[172:175], v[68:71]
	v_mfma_f32_16x16x32_bf16 v[64:67], v[148:151], v[172:175], v[64:67]
	v_mfma_f32_16x16x32_bf16 v[60:63], v[140:143], v[180:183], v[60:63]
	v_mfma_f32_16x16x32_bf16 v[56:59], v[148:151], v[180:183], v[56:59]
	v_mfma_f32_16x16x32_bf16 v[28:31], v[140:143], v[188:191], v[28:31]
	v_mfma_f32_16x16x32_bf16 v[20:23], v[148:151], v[188:191], v[20:23]
	v_mfma_f32_16x16x32_bf16 v[12:15], v[140:143], v[196:199], v[12:15]
	v_mfma_f32_16x16x32_bf16 v[8:11], v[148:151], v[196:199], v[8:11]
	v_mfma_f32_16x16x32_bf16 v[52:55], v[152:155], v[168:171], v[52:55]
	v_mfma_f32_16x16x32_bf16 v[48:51], v[160:163], v[168:171], v[48:51]
	v_mfma_f32_16x16x32_bf16 v[36:39], v[152:155], v[176:179], v[36:39]
	v_mfma_f32_16x16x32_bf16 v[16:19], v[160:163], v[176:179], v[16:19]
	v_mfma_f32_16x16x32_bf16 v[44:47], v[152:155], v[184:187], v[44:47]
	v_mfma_f32_16x16x32_bf16 v[40:43], v[160:163], v[184:187], v[40:43]
	v_mfma_f32_16x16x32_bf16 v[32:35], v[152:155], v[192:195], v[32:35]
	v_mfma_f32_16x16x32_bf16 v[24:27], v[160:163], v[192:195], v[24:27]
	v_mfma_f32_16x16x32_bf16 v[52:55], v[156:159], v[172:175], v[52:55]
	v_mfma_f32_16x16x32_bf16 v[48:51], v[164:167], v[172:175], v[48:51]
	v_mfma_f32_16x16x32_bf16 v[36:39], v[156:159], v[180:183], v[36:39]
	v_mfma_f32_16x16x32_bf16 v[16:19], v[164:167], v[180:183], v[16:19]
	v_mfma_f32_16x16x32_bf16 v[44:47], v[156:159], v[188:191], v[44:47]
	v_mfma_f32_16x16x32_bf16 v[40:43], v[164:167], v[188:191], v[40:43]
	v_mfma_f32_16x16x32_bf16 v[32:35], v[156:159], v[196:199], v[32:35]
	v_mfma_f32_16x16x32_bf16 v[24:27], v[164:167], v[196:199], v[24:27]
	s_setprio 0
	s_barrier
	s_add_i32 s49, s49, 2
	s_add_u32 s20, s20, 0x100
	s_addc_u32 s21, s21, 0
	s_add_u32 s47, s47, 0x100
	s_addc_u32 s48, s48, 0
	s_cmp_gt_u32 s49, 29
	s_cbranch_scc1 .LBB0_762

.LBB0_945:
	s_waitcnt vmcnt(8)
	s_add_u32 s8, s4, 0x80
	s_waitcnt lgkmcnt(0)
	s_addc_u32 s9, s5, 0
	s_and_b64 s[6:7], s[6:7], exec
	s_cselect_b32 s9, s13, s9
	s_cselect_b32 s8, s12, s8
	s_cselect_b32 s7, s35, s31
	s_cselect_b32 s6, s34, s29
	s_barrier
	s_setprio 1
	s_waitcnt lgkmcnt(0)
	v_mfma_scale_f32_16x16x128_f8f6f4 v[196:199], v[26:33], v[58:65], v[196:199], v1, v1 op_sel_hi:[0,0,0]
	v_mfma_scale_f32_16x16x128_f8f6f4 v[192:195], v[18:25], v[58:65], v[192:195], v1, v1 op_sel_hi:[0,0,0]
	v_mfma_scale_f32_16x16x128_f8f6f4 v[180:183], v[26:33], v[50:57], v[180:183], v1, v1 op_sel_hi:[0,0,0]
	v_mfma_scale_f32_16x16x128_f8f6f4 v[176:179], v[18:25], v[50:57], v[176:179], v1, v1 op_sel_hi:[0,0,0]
	v_mfma_scale_f32_16x16x128_f8f6f4 v[164:167], v[26:33], v[42:49], v[164:167], v1, v1 op_sel_hi:[0,0,0]
	v_mfma_scale_f32_16x16x128_f8f6f4 v[160:163], v[18:25], v[42:49], v[160:163], v1, v1 op_sel_hi:[0,0,0]
	v_mfma_scale_f32_16x16x128_f8f6f4 v[148:151], v[26:33], v[34:41], v[148:151], v1, v1 op_sel_hi:[0,0,0]
	v_mfma_scale_f32_16x16x128_f8f6f4 v[144:147], v[18:25], v[34:41], v[144:147], v1, v1 op_sel_hi:[0,0,0]
	v_mfma_scale_f32_16x16x128_f8f6f4 v[188:191], v[10:17], v[58:65], v[188:191], v1, v1 op_sel_hi:[0,0,0]
	v_mfma_scale_f32_16x16x128_f8f6f4 v[184:187], v[2:9], v[58:65], v[184:187], v1, v1 op_sel_hi:[0,0,0]
	v_mfma_scale_f32_16x16x128_f8f6f4 v[172:175], v[10:17], v[50:57], v[172:175], v1, v1 op_sel_hi:[0,0,0]
	v_mfma_scale_f32_16x16x128_f8f6f4 v[168:171], v[2:9], v[50:57], v[168:171], v1, v1 op_sel_hi:[0,0,0]
	v_mfma_scale_f32_16x16x128_f8f6f4 v[156:159], v[10:17], v[42:49], v[156:159], v1, v1 op_sel_hi:[0,0,0]
	v_mfma_scale_f32_16x16x128_f8f6f4 v[152:155], v[2:9], v[42:49], v[152:155], v1, v1 op_sel_hi:[0,0,0]
	v_mfma_scale_f32_16x16x128_f8f6f4 v[140:143], v[10:17], v[34:41], v[140:143], v1, v1 op_sel_hi:[0,0,0]
	v_mfma_scale_f32_16x16x128_f8f6f4 v[136:139], v[2:9], v[34:41], v[136:139], v1, v1 op_sel_hi:[0,0,0]
	s_setprio 0
	s_barrier
	s_mov_b32 m0, s44
	v_lshl_add_u64 v[34:35], s[6:7], 0, v[202:203]
	s_add_u32 s40, s6, 0x40000
	ds_read_b128 v[42:45], v238 offset:16384
	ds_read_b128 v[46:49], v238 offset:17408
	ds_read_b128 v[50:53], v238 offset:18432
	ds_read_b128 v[54:57], v238 offset:19456
	ds_read_b128 v[58:61], v238 offset:20480
	ds_read_b128 v[62:65], v238 offset:21504
	ds_read_b128 v[240:243], v238 offset:22528
	ds_read_b128 v[244:247], v238 offset:23552
	global_load_lds_dwordx4 v[34:35], off
	v_lshl_add_u64 v[36:37], s[6:7], 0, v[204:205]
	s_mov_b32 m0, s45
	s_addc_u32 s41, s7, 0
	global_load_lds_dwordx4 v[36:37], off
	v_lshl_add_u64 v[38:39], s[40:41], 0, v[202:203]
	s_mov_b32 m0, s46
	v_mov_b32_e32 v207, v67
	global_load_lds_dwordx4 v[38:39], off
	v_lshl_add_u64 v[38:39], s[40:41], 0, v[204:205]
	s_mov_b32 m0, s47
	v_lshl_add_u64 v[40:41], s[8:9], 0, v[66:67]
	global_load_lds_dwordx4 v[38:39], off
	s_mov_b32 m0, s37
	v_lshl_add_u64 v[38:39], s[8:9], 0, v[206:207]
	global_load_lds_dwordx4 v66, s[8:9]
	s_mov_b32 m0, s48
	s_nop 0
	global_load_lds_dwordx4 v206, s[8:9]
	s_waitcnt vmcnt(8)
	s_waitcnt lgkmcnt(0)
	s_barrier
	s_setprio 1
	s_waitcnt lgkmcnt(0)
	v_mfma_scale_f32_16x16x128_f8f6f4 v[132:135], v[26:33], v[42:49], v[132:135], v1, v1 op_sel_hi:[0,0,0]
	v_mfma_scale_f32_16x16x128_f8f6f4 v[128:131], v[18:25], v[42:49], v[128:131], v1, v1 op_sel_hi:[0,0,0]
	v_mfma_scale_f32_16x16x128_f8f6f4 v[116:119], v[26:33], v[50:57], v[116:119], v1, v1 op_sel_hi:[0,0,0]
	v_mfma_scale_f32_16x16x128_f8f6f4 v[112:115], v[18:25], v[50:57], v[112:115], v1, v1 op_sel_hi:[0,0,0]
	v_mfma_scale_f32_16x16x128_f8f6f4 v[92:95], v[26:33], v[58:65], v[92:95], v1, v1 op_sel_hi:[0,0,0]
	v_mfma_scale_f32_16x16x128_f8f6f4 v[88:91], v[18:25], v[58:65], v[88:91], v1, v1 op_sel_hi:[0,0,0]
	v_mfma_scale_f32_16x16x128_f8f6f4 v[76:79], v[26:33], v[240:247], v[76:79], v1, v1 op_sel_hi:[0,0,0]
	v_mfma_scale_f32_16x16x128_f8f6f4 v[72:75], v[18:25], v[240:247], v[72:75], v1, v1 op_sel_hi:[0,0,0]
	v_mfma_scale_f32_16x16x128_f8f6f4 v[124:127], v[10:17], v[42:49], v[124:127], v1, v1 op_sel_hi:[0,0,0]
	v_mfma_scale_f32_16x16x128_f8f6f4 v[120:123], v[2:9], v[42:49], v[120:123], v1, v1 op_sel_hi:[0,0,0]
	v_mfma_scale_f32_16x16x128_f8f6f4 v[108:111], v[10:17], v[50:57], v[108:111], v1, v1 op_sel_hi:[0,0,0]
	v_mfma_scale_f32_16x16x128_f8f6f4 v[104:107], v[2:9], v[50:57], v[104:107], v1, v1 op_sel_hi:[0,0,0]
	v_mfma_scale_f32_16x16x128_f8f6f4 v[100:103], v[10:17], v[58:65], v[100:103], v1, v1 op_sel_hi:[0,0,0]
	v_mfma_scale_f32_16x16x128_f8f6f4 v[96:99], v[2:9], v[58:65], v[96:99], v1, v1 op_sel_hi:[0,0,0]
	v_mfma_scale_f32_16x16x128_f8f6f4 v[84:87], v[10:17], v[240:247], v[84:87], v1, v1 op_sel_hi:[0,0,0]
	v_mfma_scale_f32_16x16x128_f8f6f4 v[80:83], v[2:9], v[240:247], v[80:83], v1, v1 op_sel_hi:[0,0,0]
	s_setprio 0
	s_barrier
	ds_read_b128 v[2:5], v229
	ds_read_b128 v[6:9], v230
	ds_read_b128 v[10:13], v231
	ds_read_b128 v[14:17], v232
	ds_read_b128 v[18:21], v233
	ds_read_b128 v[22:25], v234
	ds_read_b128 v[26:29], v235
	ds_read_b128 v[30:33], v236
	s_mov_b32 m0, s49
	v_lshl_add_u64 v[68:69], s[8:9], 0, v[212:213]
	ds_read_b128 v[42:45], v238 offset:32768
	ds_read_b128 v[46:49], v238 offset:33792
	ds_read_b128 v[50:53], v238 offset:34816
	ds_read_b128 v[54:57], v238 offset:35840
	ds_read_b128 v[58:61], v238 offset:36864
	ds_read_b128 v[62:65], v238 offset:37888
	ds_read_b128 v[240:243], v238 offset:38912
	ds_read_b128 v[244:247], v238 offset:39936
	global_load_lds_dwordx4 v[68:69], off
	v_lshl_add_u64 v[68:69], s[8:9], 0, v[210:211]
	s_mov_b32 m0, s50
	s_nop 0
	global_load_lds_dwordx4 v[68:69], off
	s_waitcnt vmcnt(8)
	s_waitcnt lgkmcnt(0)
	s_barrier
	s_setprio 1
	s_waitcnt lgkmcnt(0)
	v_mfma_scale_f32_16x16x128_f8f6f4 v[196:199], v[2:9], v[42:49], v[196:199], v1, v1 op_sel_hi:[0,0,0]
	v_mfma_scale_f32_16x16x128_f8f6f4 v[192:195], v[10:17], v[42:49], v[192:195], v1, v1 op_sel_hi:[0,0,0]
	v_mfma_scale_f32_16x16x128_f8f6f4 v[180:183], v[2:9], v[50:57], v[180:183], v1, v1 op_sel_hi:[0,0,0]
	v_mfma_scale_f32_16x16x128_f8f6f4 v[176:179], v[10:17], v[50:57], v[176:179], v1, v1 op_sel_hi:[0,0,0]
	v_mfma_scale_f32_16x16x128_f8f6f4 v[164:167], v[2:9], v[58:65], v[164:167], v1, v1 op_sel_hi:[0,0,0]
	v_mfma_scale_f32_16x16x128_f8f6f4 v[160:163], v[10:17], v[58:65], v[160:163], v1, v1 op_sel_hi:[0,0,0]
	v_mfma_scale_f32_16x16x128_f8f6f4 v[148:151], v[2:9], v[240:247], v[148:151], v1, v1 op_sel_hi:[0,0,0]
	v_mfma_scale_f32_16x16x128_f8f6f4 v[144:147], v[10:17], v[240:247], v[144:147], v1, v1 op_sel_hi:[0,0,0]
	v_mfma_scale_f32_16x16x128_f8f6f4 v[188:191], v[18:25], v[42:49], v[188:191], v1, v1 op_sel_hi:[0,0,0]
	v_mfma_scale_f32_16x16x128_f8f6f4 v[184:187], v[26:33], v[42:49], v[184:187], v1, v1 op_sel_hi:[0,0,0]
	v_mfma_scale_f32_16x16x128_f8f6f4 v[172:175], v[18:25], v[50:57], v[172:175], v1, v1 op_sel_hi:[0,0,0]
	v_mfma_scale_f32_16x16x128_f8f6f4 v[168:171], v[26:33], v[50:57], v[168:171], v1, v1 op_sel_hi:[0,0,0]
	v_mfma_scale_f32_16x16x128_f8f6f4 v[156:159], v[18:25], v[58:65], v[156:159], v1, v1 op_sel_hi:[0,0,0]
	v_mfma_scale_f32_16x16x128_f8f6f4 v[152:155], v[26:33], v[58:65], v[152:155], v1, v1 op_sel_hi:[0,0,0]
	v_mfma_scale_f32_16x16x128_f8f6f4 v[140:143], v[18:25], v[240:247], v[140:143], v1, v1 op_sel_hi:[0,0,0]
	v_mfma_scale_f32_16x16x128_f8f6f4 v[136:139], v[26:33], v[240:247], v[136:139], v1, v1 op_sel_hi:[0,0,0]
	s_setprio 0
	s_barrier
	s_mov_b32 m0, s53
	v_lshl_add_u64 v[34:35], v[34:35], 0, s[18:19]
	s_add_u32 s6, s6, 0x40080
	ds_read_b128 v[42:45], v238 offset:49152
	ds_read_b128 v[46:49], v238 offset:50176
	ds_read_b128 v[50:53], v238 offset:51200
	ds_read_b128 v[54:57], v238 offset:52224
	ds_read_b128 v[58:61], v238 offset:53248
	ds_read_b128 v[62:65], v238 offset:54272
	ds_read_b128 v[240:243], v238 offset:55296
	ds_read_b128 v[244:247], v238 offset:56320
	global_load_lds_dwordx4 v[34:35], off
	v_lshl_add_u64 v[34:35], v[36:37], 0, s[18:19]
	s_mov_b32 m0, s54
	s_addc_u32 s7, s7, 0
	global_load_lds_dwordx4 v[34:35], off
	v_lshl_add_u64 v[34:35], s[6:7], 0, v[202:203]
	s_mov_b32 m0, s57
	s_nop 0
	global_load_lds_dwordx4 v[34:35], off
	v_lshl_add_u64 v[34:35], s[6:7], 0, v[204:205]
	s_mov_b32 m0, s58
	s_nop 0
	global_load_lds_dwordx4 v[34:35], off
	v_lshl_add_u64 v[34:35], v[40:41], 0, s[18:19]
	s_mov_b32 m0, s55
	s_nop 0
	global_load_lds_dwordx4 v[34:35], off
	v_lshl_add_u64 v[34:35], v[38:39], 0, s[18:19]
	s_mov_b32 m0, s56
	s_nop 0
	global_load_lds_dwordx4 v[34:35], off
	s_waitcnt vmcnt(8)
	s_waitcnt lgkmcnt(0)
	s_barrier
	s_setprio 1
	s_waitcnt lgkmcnt(0)
	v_mfma_scale_f32_16x16x128_f8f6f4 v[132:135], v[2:9], v[42:49], v[132:135], v1, v1 op_sel_hi:[0,0,0]
	v_mfma_scale_f32_16x16x128_f8f6f4 v[128:131], v[10:17], v[42:49], v[128:131], v1, v1 op_sel_hi:[0,0,0]
	v_mfma_scale_f32_16x16x128_f8f6f4 v[116:119], v[2:9], v[50:57], v[116:119], v1, v1 op_sel_hi:[0,0,0]
	v_mfma_scale_f32_16x16x128_f8f6f4 v[112:115], v[10:17], v[50:57], v[112:115], v1, v1 op_sel_hi:[0,0,0]
	v_mfma_scale_f32_16x16x128_f8f6f4 v[92:95], v[2:9], v[58:65], v[92:95], v1, v1 op_sel_hi:[0,0,0]
	v_mfma_scale_f32_16x16x128_f8f6f4 v[88:91], v[10:17], v[58:65], v[88:91], v1, v1 op_sel_hi:[0,0,0]
	v_mfma_scale_f32_16x16x128_f8f6f4 v[76:79], v[2:9], v[240:247], v[76:79], v1, v1 op_sel_hi:[0,0,0]
	v_mfma_scale_f32_16x16x128_f8f6f4 v[72:75], v[10:17], v[240:247], v[72:75], v1, v1 op_sel_hi:[0,0,0]
	v_mfma_scale_f32_16x16x128_f8f6f4 v[124:127], v[18:25], v[42:49], v[124:127], v1, v1 op_sel_hi:[0,0,0]
	v_mfma_scale_f32_16x16x128_f8f6f4 v[120:123], v[26:33], v[42:49], v[120:123], v1, v1 op_sel_hi:[0,0,0]
	v_mfma_scale_f32_16x16x128_f8f6f4 v[108:111], v[18:25], v[50:57], v[108:111], v1, v1 op_sel_hi:[0,0,0]
	v_mfma_scale_f32_16x16x128_f8f6f4 v[104:107], v[26:33], v[50:57], v[104:107], v1, v1 op_sel_hi:[0,0,0]
	v_mfma_scale_f32_16x16x128_f8f6f4 v[100:103], v[18:25], v[58:65], v[100:103], v1, v1 op_sel_hi:[0,0,0]
	v_mfma_scale_f32_16x16x128_f8f6f4 v[96:99], v[26:33], v[58:65], v[96:99], v1, v1 op_sel_hi:[0,0,0]
	v_mfma_scale_f32_16x16x128_f8f6f4 v[84:87], v[18:25], v[240:247], v[84:87], v1, v1 op_sel_hi:[0,0,0]
	v_mfma_scale_f32_16x16x128_f8f6f4 v[80:83], v[26:33], v[240:247], v[80:83], v1, v1 op_sel_hi:[0,0,0]
	s_setprio 0
	s_barrier
	s_add_i32 s39, s39, 2
	s_add_u32 s4, s4, 0x100
	s_addc_u32 s5, s5, 0
	s_add_u32 s29, s29, 0x100
	s_addc_u32 s31, s31, 0
	s_cmp_gt_u32 s39, 13
	s_cbranch_scc1 .LBB0_948

.LBB0_1031:
	s_waitcnt vmcnt(8)
	s_add_u32 s44, s4, 0x80
	s_waitcnt lgkmcnt(0)
	s_addc_u32 s45, s5, 0
	s_and_b64 s[42:43], s[42:43], exec
	s_cselect_b32 s45, s7, s45
	s_cselect_b32 s44, s6, s44
	s_cselect_b32 s43, s39, s35
	s_cselect_b32 s42, s38, s31
	s_barrier
	s_setprio 1
	s_waitcnt lgkmcnt(0)
	v_mfma_scale_f32_16x16x128_f8f6f4 v[196:199], v[26:33], v[58:65], v[196:199], v1, v1 op_sel_hi:[0,0,0]
	v_mfma_scale_f32_16x16x128_f8f6f4 v[192:195], v[18:25], v[58:65], v[192:195], v1, v1 op_sel_hi:[0,0,0]
	v_mfma_scale_f32_16x16x128_f8f6f4 v[188:191], v[26:33], v[50:57], v[188:191], v1, v1 op_sel_hi:[0,0,0]
	v_mfma_scale_f32_16x16x128_f8f6f4 v[184:187], v[18:25], v[50:57], v[184:187], v1, v1 op_sel_hi:[0,0,0]
	v_mfma_scale_f32_16x16x128_f8f6f4 v[180:183], v[26:33], v[42:49], v[180:183], v1, v1 op_sel_hi:[0,0,0]
	v_mfma_scale_f32_16x16x128_f8f6f4 v[172:175], v[18:25], v[42:49], v[172:175], v1, v1 op_sel_hi:[0,0,0]
	v_mfma_scale_f32_16x16x128_f8f6f4 v[148:151], v[26:33], v[34:41], v[148:151], v1, v1 op_sel_hi:[0,0,0]
	v_mfma_scale_f32_16x16x128_f8f6f4 v[144:147], v[18:25], v[34:41], v[144:147], v1, v1 op_sel_hi:[0,0,0]
	v_mfma_scale_f32_16x16x128_f8f6f4 v[176:179], v[10:17], v[58:65], v[176:179], v1, v1 op_sel_hi:[0,0,0]
	v_mfma_scale_f32_16x16x128_f8f6f4 v[168:171], v[2:9], v[58:65], v[168:171], v1, v1 op_sel_hi:[0,0,0]
	v_mfma_scale_f32_16x16x128_f8f6f4 v[164:167], v[10:17], v[50:57], v[164:167], v1, v1 op_sel_hi:[0,0,0]
	v_mfma_scale_f32_16x16x128_f8f6f4 v[160:163], v[2:9], v[50:57], v[160:163], v1, v1 op_sel_hi:[0,0,0]
	v_mfma_scale_f32_16x16x128_f8f6f4 v[156:159], v[10:17], v[42:49], v[156:159], v1, v1 op_sel_hi:[0,0,0]
	v_mfma_scale_f32_16x16x128_f8f6f4 v[152:155], v[2:9], v[42:49], v[152:155], v1, v1 op_sel_hi:[0,0,0]
	v_mfma_scale_f32_16x16x128_f8f6f4 v[140:143], v[10:17], v[34:41], v[140:143], v1, v1 op_sel_hi:[0,0,0]
	v_mfma_scale_f32_16x16x128_f8f6f4 v[136:139], v[2:9], v[34:41], v[136:139], v1, v1 op_sel_hi:[0,0,0]
	s_setprio 0
	s_barrier
	s_mov_b32 m0, s47
	v_lshl_add_u64 v[34:35], s[42:43], 0, v[202:203]
	s_add_u32 s68, s42, 0x40000
	ds_read_b128 v[42:45], v237 offset:16384
	ds_read_b128 v[46:49], v237 offset:17408
	ds_read_b128 v[50:53], v237 offset:18432
	ds_read_b128 v[54:57], v237 offset:19456
	ds_read_b128 v[58:61], v237 offset:20480
	ds_read_b128 v[62:65], v237 offset:21504
	ds_read_b128 v[238:241], v237 offset:22528
	ds_read_b128 v[242:245], v237 offset:23552
	global_load_lds_dwordx4 v[34:35], off
	v_lshl_add_u64 v[36:37], s[42:43], 0, v[204:205]
	s_mov_b32 m0, s48
	s_addc_u32 s69, s43, 0
	global_load_lds_dwordx4 v[36:37], off
	v_lshl_add_u64 v[38:39], s[68:69], 0, v[202:203]
	s_mov_b32 m0, s49
	v_mov_b32_e32 v207, v67
	global_load_lds_dwordx4 v[38:39], off
	v_lshl_add_u64 v[38:39], s[68:69], 0, v[204:205]
	s_mov_b32 m0, s50
	v_lshl_add_u64 v[40:41], s[44:45], 0, v[66:67]
	global_load_lds_dwordx4 v[38:39], off
	s_mov_b32 m0, s37
	v_lshl_add_u64 v[38:39], s[44:45], 0, v[206:207]
	global_load_lds_dwordx4 v66, s[44:45]
	s_mov_b32 m0, s51
	s_nop 0
	global_load_lds_dwordx4 v206, s[44:45]
	s_waitcnt vmcnt(8)
	s_waitcnt lgkmcnt(0)
	s_barrier
	s_setprio 1
	s_waitcnt lgkmcnt(0)
	v_mfma_scale_f32_16x16x128_f8f6f4 v[132:135], v[26:33], v[42:49], v[132:135], v1, v1 op_sel_hi:[0,0,0]
	v_mfma_scale_f32_16x16x128_f8f6f4 v[128:131], v[18:25], v[42:49], v[128:131], v1, v1 op_sel_hi:[0,0,0]
	v_mfma_scale_f32_16x16x128_f8f6f4 v[116:119], v[26:33], v[50:57], v[116:119], v1, v1 op_sel_hi:[0,0,0]
	v_mfma_scale_f32_16x16x128_f8f6f4 v[104:107], v[18:25], v[50:57], v[104:107], v1, v1 op_sel_hi:[0,0,0]
	v_mfma_scale_f32_16x16x128_f8f6f4 v[88:91], v[26:33], v[58:65], v[88:91], v1, v1 op_sel_hi:[0,0,0]
	v_mfma_scale_f32_16x16x128_f8f6f4 v[84:87], v[18:25], v[58:65], v[84:87], v1, v1 op_sel_hi:[0,0,0]
	v_mfma_scale_f32_16x16x128_f8f6f4 v[76:79], v[26:33], v[238:245], v[76:79], v1, v1 op_sel_hi:[0,0,0]
	v_mfma_scale_f32_16x16x128_f8f6f4 v[72:75], v[18:25], v[238:245], v[72:75], v1, v1 op_sel_hi:[0,0,0]
	v_mfma_scale_f32_16x16x128_f8f6f4 v[124:127], v[10:17], v[42:49], v[124:127], v1, v1 op_sel_hi:[0,0,0]
	v_mfma_scale_f32_16x16x128_f8f6f4 v[108:111], v[2:9], v[42:49], v[108:111], v1, v1 op_sel_hi:[0,0,0]
	v_mfma_scale_f32_16x16x128_f8f6f4 v[92:95], v[10:17], v[50:57], v[92:95], v1, v1 op_sel_hi:[0,0,0]
	v_mfma_scale_f32_16x16x128_f8f6f4 v[80:83], v[2:9], v[50:57], v[80:83], v1, v1 op_sel_hi:[0,0,0]
	v_mfma_scale_f32_16x16x128_f8f6f4 v[112:115], v[10:17], v[58:65], v[112:115], v1, v1 op_sel_hi:[0,0,0]
	v_mfma_scale_f32_16x16x128_f8f6f4 v[120:123], v[2:9], v[58:65], v[120:123], v1, v1 op_sel_hi:[0,0,0]
	v_mfma_scale_f32_16x16x128_f8f6f4 v[96:99], v[10:17], v[238:245], v[96:99], v1, v1 op_sel_hi:[0,0,0]
	v_mfma_scale_f32_16x16x128_f8f6f4 v[100:103], v[2:9], v[238:245], v[100:103], v1, v1 op_sel_hi:[0,0,0]
	s_setprio 0
	s_barrier
	ds_read_b128 v[2:5], v224
	ds_read_b128 v[6:9], v225
	ds_read_b128 v[10:13], v226
	ds_read_b128 v[14:17], v227
	ds_read_b128 v[18:21], v228
	ds_read_b128 v[22:25], v229
	ds_read_b128 v[26:29], v230
	ds_read_b128 v[30:33], v231
	s_mov_b32 m0, s52
	v_lshl_add_u64 v[68:69], s[44:45], 0, v[212:213]
	ds_read_b128 v[42:45], v237 offset:32768
	ds_read_b128 v[46:49], v237 offset:33792
	ds_read_b128 v[50:53], v237 offset:34816
	ds_read_b128 v[54:57], v237 offset:35840
	ds_read_b128 v[58:61], v237 offset:36864
	ds_read_b128 v[62:65], v237 offset:37888
	ds_read_b128 v[238:241], v237 offset:38912
	ds_read_b128 v[242:245], v237 offset:39936
	global_load_lds_dwordx4 v[68:69], off
	v_lshl_add_u64 v[68:69], s[44:45], 0, v[210:211]
	s_mov_b32 m0, s53
	s_nop 0
	global_load_lds_dwordx4 v[68:69], off
	s_waitcnt vmcnt(8)
	s_waitcnt lgkmcnt(0)
	s_barrier
	s_setprio 1
	s_waitcnt lgkmcnt(0)
	v_mfma_scale_f32_16x16x128_f8f6f4 v[196:199], v[2:9], v[42:49], v[196:199], v1, v1 op_sel_hi:[0,0,0]
	v_mfma_scale_f32_16x16x128_f8f6f4 v[192:195], v[10:17], v[42:49], v[192:195], v1, v1 op_sel_hi:[0,0,0]
	v_mfma_scale_f32_16x16x128_f8f6f4 v[188:191], v[2:9], v[50:57], v[188:191], v1, v1 op_sel_hi:[0,0,0]
	v_mfma_scale_f32_16x16x128_f8f6f4 v[184:187], v[10:17], v[50:57], v[184:187], v1, v1 op_sel_hi:[0,0,0]
	v_mfma_scale_f32_16x16x128_f8f6f4 v[180:183], v[2:9], v[58:65], v[180:183], v1, v1 op_sel_hi:[0,0,0]
	v_mfma_scale_f32_16x16x128_f8f6f4 v[172:175], v[10:17], v[58:65], v[172:175], v1, v1 op_sel_hi:[0,0,0]
	v_mfma_scale_f32_16x16x128_f8f6f4 v[148:151], v[2:9], v[238:245], v[148:151], v1, v1 op_sel_hi:[0,0,0]
	v_mfma_scale_f32_16x16x128_f8f6f4 v[144:147], v[10:17], v[238:245], v[144:147], v1, v1 op_sel_hi:[0,0,0]
	v_mfma_scale_f32_16x16x128_f8f6f4 v[176:179], v[18:25], v[42:49], v[176:179], v1, v1 op_sel_hi:[0,0,0]
	v_mfma_scale_f32_16x16x128_f8f6f4 v[168:171], v[26:33], v[42:49], v[168:171], v1, v1 op_sel_hi:[0,0,0]
	v_mfma_scale_f32_16x16x128_f8f6f4 v[164:167], v[18:25], v[50:57], v[164:167], v1, v1 op_sel_hi:[0,0,0]
	v_mfma_scale_f32_16x16x128_f8f6f4 v[160:163], v[26:33], v[50:57], v[160:163], v1, v1 op_sel_hi:[0,0,0]
	v_mfma_scale_f32_16x16x128_f8f6f4 v[156:159], v[18:25], v[58:65], v[156:159], v1, v1 op_sel_hi:[0,0,0]
	v_mfma_scale_f32_16x16x128_f8f6f4 v[152:155], v[26:33], v[58:65], v[152:155], v1, v1 op_sel_hi:[0,0,0]
	v_mfma_scale_f32_16x16x128_f8f6f4 v[140:143], v[18:25], v[238:245], v[140:143], v1, v1 op_sel_hi:[0,0,0]
	v_mfma_scale_f32_16x16x128_f8f6f4 v[136:139], v[26:33], v[238:245], v[136:139], v1, v1 op_sel_hi:[0,0,0]
	s_setprio 0
	s_barrier
	s_mov_b32 m0, s56
	v_lshl_add_u64 v[34:35], v[34:35], 0, s[14:15]
	s_add_u32 s42, s42, 0x40080
	ds_read_b128 v[42:45], v237 offset:49152
	ds_read_b128 v[46:49], v237 offset:50176
	ds_read_b128 v[50:53], v237 offset:51200
	ds_read_b128 v[54:57], v237 offset:52224
	ds_read_b128 v[58:61], v237 offset:53248
	ds_read_b128 v[62:65], v237 offset:54272
	ds_read_b128 v[238:241], v237 offset:55296
	ds_read_b128 v[242:245], v237 offset:56320
	global_load_lds_dwordx4 v[34:35], off
	v_lshl_add_u64 v[34:35], v[36:37], 0, s[14:15]
	s_mov_b32 m0, s57
	s_addc_u32 s43, s43, 0
	global_load_lds_dwordx4 v[34:35], off
	v_lshl_add_u64 v[34:35], s[42:43], 0, v[202:203]
	s_mov_b32 m0, s60
	s_nop 0
	global_load_lds_dwordx4 v[34:35], off
	v_lshl_add_u64 v[34:35], s[42:43], 0, v[204:205]
	s_mov_b32 m0, s61
	s_nop 0
	global_load_lds_dwordx4 v[34:35], off
	v_lshl_add_u64 v[34:35], v[40:41], 0, s[14:15]
	s_mov_b32 m0, s58
	s_nop 0
	global_load_lds_dwordx4 v[34:35], off
	v_lshl_add_u64 v[34:35], v[38:39], 0, s[14:15]
	s_mov_b32 m0, s59
	s_nop 0
	global_load_lds_dwordx4 v[34:35], off
	s_waitcnt vmcnt(8)
	s_waitcnt lgkmcnt(0)
	s_barrier
	s_setprio 1
	s_waitcnt lgkmcnt(0)
	v_mfma_scale_f32_16x16x128_f8f6f4 v[132:135], v[2:9], v[42:49], v[132:135], v1, v1 op_sel_hi:[0,0,0]
	v_mfma_scale_f32_16x16x128_f8f6f4 v[128:131], v[10:17], v[42:49], v[128:131], v1, v1 op_sel_hi:[0,0,0]
	v_mfma_scale_f32_16x16x128_f8f6f4 v[116:119], v[2:9], v[50:57], v[116:119], v1, v1 op_sel_hi:[0,0,0]
	v_mfma_scale_f32_16x16x128_f8f6f4 v[104:107], v[10:17], v[50:57], v[104:107], v1, v1 op_sel_hi:[0,0,0]
	v_mfma_scale_f32_16x16x128_f8f6f4 v[88:91], v[2:9], v[58:65], v[88:91], v1, v1 op_sel_hi:[0,0,0]
	v_mfma_scale_f32_16x16x128_f8f6f4 v[84:87], v[10:17], v[58:65], v[84:87], v1, v1 op_sel_hi:[0,0,0]
	v_mfma_scale_f32_16x16x128_f8f6f4 v[76:79], v[2:9], v[238:245], v[76:79], v1, v1 op_sel_hi:[0,0,0]
	v_mfma_scale_f32_16x16x128_f8f6f4 v[72:75], v[10:17], v[238:245], v[72:75], v1, v1 op_sel_hi:[0,0,0]
	v_mfma_scale_f32_16x16x128_f8f6f4 v[124:127], v[18:25], v[42:49], v[124:127], v1, v1 op_sel_hi:[0,0,0]
	v_mfma_scale_f32_16x16x128_f8f6f4 v[108:111], v[26:33], v[42:49], v[108:111], v1, v1 op_sel_hi:[0,0,0]
	v_mfma_scale_f32_16x16x128_f8f6f4 v[92:95], v[18:25], v[50:57], v[92:95], v1, v1 op_sel_hi:[0,0,0]
	v_mfma_scale_f32_16x16x128_f8f6f4 v[80:83], v[26:33], v[50:57], v[80:83], v1, v1 op_sel_hi:[0,0,0]
	v_mfma_scale_f32_16x16x128_f8f6f4 v[112:115], v[18:25], v[58:65], v[112:115], v1, v1 op_sel_hi:[0,0,0]
	v_mfma_scale_f32_16x16x128_f8f6f4 v[120:123], v[26:33], v[58:65], v[120:123], v1, v1 op_sel_hi:[0,0,0]
	v_mfma_scale_f32_16x16x128_f8f6f4 v[96:99], v[18:25], v[238:245], v[96:99], v1, v1 op_sel_hi:[0,0,0]
	v_mfma_scale_f32_16x16x128_f8f6f4 v[100:103], v[26:33], v[238:245], v[100:103], v1, v1 op_sel_hi:[0,0,0]
	s_setprio 0
	s_barrier
	s_add_i32 s41, s41, 2
	s_add_u32 s4, s4, 0x100
	s_addc_u32 s5, s5, 0
	s_add_u32 s31, s31, 0x100
	s_addc_u32 s35, s35, 0
	s_cmp_gt_u32 s41, 13
	s_cbranch_scc1 .LBB0_1034
